# G2 fp8 GEMM K-loops: both A-side fragment pairs of a K-tile kept resident in 16 spare VGPRs so each is read from LDS once per K-tile (24 instead of 32 ds_read_b128 per K-tile per wave)
# baseline (speedup 1.0000x reference)
.LBB0_1060:
	v_mov_b32_e32 v137, v133
	v_mov_b32_e32 v139, v133
	s_mov_b64 s[44:45], 0
	s_mov_b64 s[40:41], -1
	s_mov_b64 s[42:43], 0
	s_add_u32 s52, s12, s44
	s_addc_u32 s53, s13, s45
	s_add_u32 s29, s52, 0x100
	s_addc_u32 s48, s53, 0
	s_and_b64 s[46:47], s[42:43], exec
	s_cselect_b32 s46, s12, s29
	s_cselect_b32 s47, s13, s48
	s_add_u32 s29, s38, s44
	s_addc_u32 s44, s39, s45
	s_add_u32 s29, s29, 0x100
	s_addc_u32 s48, s44, 0
	ds_read_b128 v[162:165], v147
	ds_read_b128 v[170:173], v147 offset:2048
	ds_read_b128 v[166:169], v148
	ds_read_b128 v[174:177], v148 offset:2048
	s_and_b64 s[44:45], s[42:43], exec
	s_cselect_b32 s51, s35, s48
	s_cselect_b32 s50, s34, s29
	s_add_i32 m0, s0, 0xc000
	s_add_i32 s29, s0, 0xe000
	s_add_u32 s48, s50, 0x1000
	s_addc_u32 s49, s51, 0
	s_add_u32 s44, s50, 0x1080
	s_addc_u32 s45, s51, 0
	v_cndmask_b32_e64 v132, v135, v157, s[42:43]
	v_cndmask_b32_e64 v161, v136, v159, s[42:43]
	v_lshl_add_u64 v[140:141], s[52:53], 0, v[136:137]
	v_lshl_add_u64 v[140:141], v[140:141], 0, s[20:21]
	ds_read_b128 v[178:181], v145
	ds_read_b128 v[186:189], v145 offset:2048
	ds_read_b128 v[182:185], v146
	ds_read_b128 v[190:193], v146 offset:2048
	ds_read_b128 v[196:199], v145 offset:4096
	ds_read_b128 v[204:207], v145 offset:6144
	ds_read_b128 v[200:203], v146 offset:4096
	ds_read_b128 v[208:211], v146 offset:6144
	global_load_lds_dwordx4 v[140:141], off
	v_lshl_add_u64 v[140:141], s[52:53], 0, v[138:139]
	v_lshl_add_u64 v[140:141], v[140:141], 0, s[20:21]
	s_mov_b32 m0, s29
	s_nop 0
	global_load_lds_dwordx4 v[140:141], off
	s_waitcnt lgkmcnt(8)
	s_barrier
	s_waitcnt lgkmcnt(0)
	v_cndmask_b32_e64 v140, v134, v158, s[42:43]
	s_setprio 1
	s_waitcnt lgkmcnt(0)
	v_mfma_f32_16x16x128_f8f6f4 v[124:127], v[162:169], v[178:185], 0
	v_mfma_f32_16x16x128_f8f6f4 v[120:123], v[170:177], v[178:185], 0
	v_mfma_f32_16x16x128_f8f6f4 v[108:111], v[162:169], v[186:193], 0
	v_mfma_f32_16x16x128_f8f6f4 v[104:107], v[170:177], v[186:193], 0
	v_mfma_f32_16x16x128_f8f6f4 v[92:95], v[162:169], v[196:203], 0
	v_mfma_f32_16x16x128_f8f6f4 v[88:91], v[170:177], v[196:203], 0
	v_mfma_f32_16x16x128_f8f6f4 v[76:79], v[162:169], v[204:211], 0
	v_mfma_f32_16x16x128_f8f6f4 v[72:75], v[170:177], v[204:211], 0
	s_setprio 0
	s_barrier
	ds_read_b128 v[218:221], v147 offset:16384
	ds_read_b128 v[226:229], v147 offset:18432
	ds_read_b128 v[222:225], v148 offset:16384
	ds_read_b128 v[230:233], v148 offset:18432
	s_barrier
	s_waitcnt lgkmcnt(0)
	s_setprio 1
	s_waitcnt lgkmcnt(0)
	v_mfma_f32_16x16x128_f8f6f4 v[116:119], v[218:225], v[178:185], 0
	v_mfma_f32_16x16x128_f8f6f4 v[112:115], v[226:233], v[178:185], 0
	v_mfma_f32_16x16x128_f8f6f4 v[100:103], v[218:225], v[186:193], 0
	v_mfma_f32_16x16x128_f8f6f4 v[96:99], v[226:233], v[186:193], 0
	v_mfma_f32_16x16x128_f8f6f4 v[84:87], v[218:225], v[196:203], 0
	v_mfma_f32_16x16x128_f8f6f4 v[80:83], v[226:233], v[196:203], 0
	v_mfma_f32_16x16x128_f8f6f4 v[68:71], v[218:225], v[204:211], 0
	v_mfma_f32_16x16x128_f8f6f4 v[64:67], v[226:233], v[204:211], 0
	s_setprio 0
	s_barrier
	s_mov_b32 m0, s0
	ds_read_b128 v[178:181], v145 offset:16384
	ds_read_b128 v[186:189], v145 offset:18432
	ds_read_b128 v[182:185], v146 offset:16384
	ds_read_b128 v[190:193], v146 offset:18432
	ds_read_b128 v[196:199], v145 offset:20480
	ds_read_b128 v[204:207], v145 offset:22528
	ds_read_b128 v[200:203], v146 offset:20480
	ds_read_b128 v[208:211], v146 offset:22528
	global_load_lds_dwordx4 v132, s[46:47]
	s_mov_b32 m0, s56
	v_mov_b32_e32 v141, v133
	global_load_lds_dwordx4 v140, s[46:47]
	s_waitcnt lgkmcnt(8)
	s_barrier
	s_waitcnt lgkmcnt(0)
	v_lshl_add_u64 v[212:213], s[46:47], 0, v[132:133]
	v_lshl_add_u64 v[214:215], s[46:47], 0, v[140:141]
	s_setprio 1
	s_waitcnt lgkmcnt(0)
	v_mfma_f32_16x16x128_f8f6f4 v[60:63], v[162:169], v[178:185], 0
	v_mfma_f32_16x16x128_f8f6f4 v[56:59], v[170:177], v[178:185], 0
	v_mfma_f32_16x16x128_f8f6f4 v[44:47], v[162:169], v[186:193], 0
	v_mfma_f32_16x16x128_f8f6f4 v[40:43], v[170:177], v[186:193], 0
	v_mfma_f32_16x16x128_f8f6f4 v[28:31], v[162:169], v[196:203], 0
	v_mfma_f32_16x16x128_f8f6f4 v[24:27], v[170:177], v[196:203], 0
	v_mfma_f32_16x16x128_f8f6f4 v[12:15], v[162:169], v[204:211], 0
	v_mfma_f32_16x16x128_f8f6f4 v[8:11], v[170:177], v[204:211], 0
	s_setprio 0
	s_barrier
	s_mov_b32 m0, s1
	v_lshl_add_u64 v[140:141], s[50:51], 0, v[128:129]
	global_load_lds_dwordx4 v[140:141], off
	v_lshl_add_u64 v[142:143], s[50:51], 0, v[130:131]
	s_mov_b32 m0, s37
	s_nop 0
	global_load_lds_dwordx4 v[142:143], off
	s_waitcnt vmcnt(4)
	s_waitcnt lgkmcnt(0)
	s_barrier
	s_setprio 1
	s_waitcnt lgkmcnt(0)
	v_mfma_f32_16x16x128_f8f6f4 v[52:55], v[218:225], v[178:185], 0
	v_mfma_f32_16x16x128_f8f6f4 v[48:51], v[226:233], v[178:185], 0
	v_mfma_f32_16x16x128_f8f6f4 v[36:39], v[218:225], v[186:193], 0
	v_mfma_f32_16x16x128_f8f6f4 v[32:35], v[226:233], v[186:193], 0
	v_mfma_f32_16x16x128_f8f6f4 v[20:23], v[218:225], v[196:203], 0
	v_mfma_f32_16x16x128_f8f6f4 v[16:19], v[226:233], v[196:203], 0
	v_mfma_f32_16x16x128_f8f6f4 v[4:7], v[218:225], v[204:211], 0
	v_mfma_f32_16x16x128_f8f6f4 v[0:3], v[226:233], v[204:211], 0
	s_setprio 0
	s_barrier
	ds_read_b128 v[162:165], v147 offset:32768
	ds_read_b128 v[170:173], v147 offset:34816
	ds_read_b128 v[166:169], v148 offset:32768
	ds_read_b128 v[174:177], v148 offset:34816
	s_mov_b32 m0, s63
	ds_read_b128 v[178:181], v145 offset:32768
	ds_read_b128 v[186:189], v145 offset:34816
	ds_read_b128 v[182:185], v146 offset:32768
	ds_read_b128 v[190:193], v146 offset:34816
	ds_read_b128 v[196:199], v145 offset:36864
	ds_read_b128 v[204:207], v145 offset:38912
	ds_read_b128 v[200:203], v146 offset:36864
	ds_read_b128 v[208:211], v146 offset:38912
	v_cndmask_b32_e64 v132, v138, v160, s[42:43]
	global_load_lds_dwordx4 v161, s[46:47]
	s_mov_b32 m0, s64
	v_lshl_add_u64 v[216:217], s[48:49], 0, v[128:129]
	global_load_lds_dwordx4 v132, s[46:47]
	s_mov_b32 m0, s57
	s_nop 0
	global_load_lds_dwordx4 v[216:217], off
	v_lshl_add_u64 v[216:217], s[48:49], 0, v[130:131]
	s_mov_b32 m0, s62
	s_nop 0
	global_load_lds_dwordx4 v[216:217], off
	s_waitcnt lgkmcnt(8)
	s_barrier
	s_waitcnt lgkmcnt(0)
	s_setprio 1
	s_waitcnt lgkmcnt(0)
	v_mfma_f32_16x16x128_f8f6f4 v[124:127], v[162:169], v[178:185], v[124:127]
	v_mfma_f32_16x16x128_f8f6f4 v[120:123], v[170:177], v[178:185], v[120:123]
	v_mfma_f32_16x16x128_f8f6f4 v[108:111], v[162:169], v[186:193], v[108:111]
	v_mfma_f32_16x16x128_f8f6f4 v[104:107], v[170:177], v[186:193], v[104:107]
	v_mfma_f32_16x16x128_f8f6f4 v[92:95], v[162:169], v[196:203], v[92:95]
	v_mfma_f32_16x16x128_f8f6f4 v[88:91], v[170:177], v[196:203], v[88:91]
	v_mfma_f32_16x16x128_f8f6f4 v[76:79], v[162:169], v[204:211], v[76:79]
	v_mfma_f32_16x16x128_f8f6f4 v[72:75], v[170:177], v[204:211], v[72:75]
	s_setprio 0
	s_barrier
	ds_read_b128 v[218:221], v147 offset:49152
	ds_read_b128 v[226:229], v147 offset:51200
	ds_read_b128 v[222:225], v148 offset:49152
	ds_read_b128 v[230:233], v148 offset:51200
	s_barrier
	s_waitcnt lgkmcnt(0)
	s_setprio 1
	s_waitcnt lgkmcnt(0)
	v_mfma_f32_16x16x128_f8f6f4 v[116:119], v[218:225], v[178:185], v[116:119]
	v_mfma_f32_16x16x128_f8f6f4 v[112:115], v[226:233], v[178:185], v[112:115]
	v_mfma_f32_16x16x128_f8f6f4 v[100:103], v[218:225], v[186:193], v[100:103]
	v_mfma_f32_16x16x128_f8f6f4 v[96:99], v[226:233], v[186:193], v[96:99]
	v_mfma_f32_16x16x128_f8f6f4 v[84:87], v[218:225], v[196:203], v[84:87]
	v_mfma_f32_16x16x128_f8f6f4 v[80:83], v[226:233], v[196:203], v[80:83]
	v_mfma_f32_16x16x128_f8f6f4 v[68:71], v[218:225], v[204:211], v[68:71]
	v_mfma_f32_16x16x128_f8f6f4 v[64:67], v[226:233], v[204:211], v[64:67]
	s_setprio 0
	s_barrier
	s_mov_b32 m0, s67
	v_lshl_add_u64 v[212:213], v[212:213], 0, s[20:21]
	ds_read_b128 v[178:181], v145 offset:49152
	ds_read_b128 v[186:189], v145 offset:51200
	ds_read_b128 v[182:185], v146 offset:49152
	ds_read_b128 v[190:193], v146 offset:51200
	ds_read_b128 v[196:199], v145 offset:53248
	ds_read_b128 v[204:207], v145 offset:55296
	ds_read_b128 v[200:203], v146 offset:53248
	ds_read_b128 v[208:211], v146 offset:55296
	global_load_lds_dwordx4 v[212:213], off
	v_lshl_add_u64 v[212:213], v[214:215], 0, s[20:21]
	s_mov_b32 m0, s68
	s_nop 0
	global_load_lds_dwordx4 v[212:213], off
	s_waitcnt lgkmcnt(8)
	s_barrier
	s_waitcnt lgkmcnt(0)
	s_setprio 1
	s_waitcnt lgkmcnt(0)
	v_mfma_f32_16x16x128_f8f6f4 v[60:63], v[162:169], v[178:185], v[60:63]
	v_mfma_f32_16x16x128_f8f6f4 v[56:59], v[170:177], v[178:185], v[56:59]
	v_mfma_f32_16x16x128_f8f6f4 v[44:47], v[162:169], v[186:193], v[44:47]
	v_mfma_f32_16x16x128_f8f6f4 v[40:43], v[170:177], v[186:193], v[40:43]
	v_mfma_f32_16x16x128_f8f6f4 v[28:31], v[162:169], v[196:203], v[28:31]
	v_mfma_f32_16x16x128_f8f6f4 v[24:27], v[170:177], v[196:203], v[24:27]
	v_mfma_f32_16x16x128_f8f6f4 v[12:15], v[162:169], v[204:211], v[12:15]
	v_mfma_f32_16x16x128_f8f6f4 v[8:11], v[170:177], v[204:211], v[8:11]
	s_setprio 0
	s_barrier
	s_mov_b32 m0, s65
	v_lshl_add_u64 v[140:141], v[140:141], 0, s[20:21]
	global_load_lds_dwordx4 v[140:141], off
	v_lshl_add_u64 v[140:141], v[142:143], 0, s[20:21]
	s_mov_b32 m0, s66
	s_nop 0
	global_load_lds_dwordx4 v[140:141], off
	s_waitcnt vmcnt(4)
	s_waitcnt lgkmcnt(0)
	s_barrier
	s_setprio 1
	s_waitcnt lgkmcnt(0)
	v_mfma_f32_16x16x128_f8f6f4 v[52:55], v[218:225], v[178:185], v[52:55]
	v_mfma_f32_16x16x128_f8f6f4 v[48:51], v[226:233], v[178:185], v[48:51]
	v_mfma_f32_16x16x128_f8f6f4 v[36:39], v[218:225], v[186:193], v[36:39]
	v_mfma_f32_16x16x128_f8f6f4 v[32:35], v[226:233], v[186:193], v[32:35]
	v_mfma_f32_16x16x128_f8f6f4 v[20:23], v[218:225], v[196:203], v[20:23]
	v_mfma_f32_16x16x128_f8f6f4 v[16:19], v[226:233], v[196:203], v[16:19]
	v_mfma_f32_16x16x128_f8f6f4 v[4:7], v[218:225], v[204:211], v[4:7]
	v_mfma_f32_16x16x128_f8f6f4 v[0:3], v[226:233], v[204:211], v[0:3]
	s_setprio 0
	s_barrier
	s_mov_b32 m0, s69
	v_lshl_add_u64 v[140:141], s[44:45], 0, v[128:129]
	global_load_lds_dwordx4 v[140:141], off
	v_lshl_add_u64 v[140:141], s[44:45], 0, v[130:131]
	s_mov_b32 m0, s70
	s_andn2_b64 vcc, exec, s[40:41]
	global_load_lds_dwordx4 v[140:141], off
	s_mov_b64 s[42:43], -1
	s_mov_b64 s[40:41], 0
	s_mov_b64 s[44:45], 0x100
	s_cbranch_vccz .LBB0_1061
	s_branch .Lpeel_after_1061
.LBB0_1061:
	s_add_u32 s52, s12, s44
	s_addc_u32 s53, s13, s45
	s_add_u32 s29, s52, 0x100
	s_addc_u32 s48, s53, 0
	s_and_b64 s[46:47], s[42:43], exec
	s_cselect_b32 s46, s12, s29
	s_cselect_b32 s47, s13, s48
	s_add_u32 s29, s38, s44
	s_addc_u32 s44, s39, s45
	s_add_u32 s29, s29, 0x100
	s_addc_u32 s48, s44, 0
	ds_read_b128 v[162:165], v147
	ds_read_b128 v[170:173], v147 offset:2048
	ds_read_b128 v[166:169], v148
	ds_read_b128 v[174:177], v148 offset:2048
	s_and_b64 s[44:45], s[42:43], exec
	s_cselect_b32 s51, s35, s48
	s_cselect_b32 s50, s34, s29
	s_add_i32 m0, s0, 0xc000
	s_add_i32 s29, s0, 0xe000
	s_add_u32 s48, s50, 0x1000
	s_addc_u32 s49, s51, 0
	s_add_u32 s44, s50, 0x1080
	s_addc_u32 s45, s51, 0
	v_cndmask_b32_e64 v132, v135, v157, s[42:43]
	v_cndmask_b32_e64 v161, v136, v159, s[42:43]
	v_lshl_add_u64 v[140:141], s[52:53], 0, v[136:137]
	v_lshl_add_u64 v[140:141], v[140:141], 0, s[20:21]
	ds_read_b128 v[178:181], v145
	ds_read_b128 v[186:189], v145 offset:2048
	ds_read_b128 v[182:185], v146
	ds_read_b128 v[190:193], v146 offset:2048
	ds_read_b128 v[196:199], v145 offset:4096
	ds_read_b128 v[204:207], v145 offset:6144
	ds_read_b128 v[200:203], v146 offset:4096
	ds_read_b128 v[208:211], v146 offset:6144
	global_load_lds_dwordx4 v[140:141], off
	v_lshl_add_u64 v[140:141], s[52:53], 0, v[138:139]
	v_lshl_add_u64 v[140:141], v[140:141], 0, s[20:21]
	s_mov_b32 m0, s29
	s_nop 0
	global_load_lds_dwordx4 v[140:141], off
	s_waitcnt lgkmcnt(8)
	s_barrier
	s_waitcnt lgkmcnt(0)
	v_cndmask_b32_e64 v140, v134, v158, s[42:43]
	s_setprio 1
	s_waitcnt lgkmcnt(0)
	v_mfma_f32_16x16x128_f8f6f4 v[124:127], v[162:169], v[178:185], v[124:127]
	v_mfma_f32_16x16x128_f8f6f4 v[120:123], v[170:177], v[178:185], v[120:123]
	v_mfma_f32_16x16x128_f8f6f4 v[108:111], v[162:169], v[186:193], v[108:111]
	v_mfma_f32_16x16x128_f8f6f4 v[104:107], v[170:177], v[186:193], v[104:107]
	v_mfma_f32_16x16x128_f8f6f4 v[92:95], v[162:169], v[196:203], v[92:95]
	v_mfma_f32_16x16x128_f8f6f4 v[88:91], v[170:177], v[196:203], v[88:91]
	v_mfma_f32_16x16x128_f8f6f4 v[76:79], v[162:169], v[204:211], v[76:79]
	v_mfma_f32_16x16x128_f8f6f4 v[72:75], v[170:177], v[204:211], v[72:75]
	s_setprio 0
	s_barrier
	ds_read_b128 v[218:221], v147 offset:16384
	ds_read_b128 v[226:229], v147 offset:18432
	ds_read_b128 v[222:225], v148 offset:16384
	ds_read_b128 v[230:233], v148 offset:18432
	s_barrier
	s_waitcnt lgkmcnt(0)
	s_setprio 1
	s_waitcnt lgkmcnt(0)
	v_mfma_f32_16x16x128_f8f6f4 v[116:119], v[218:225], v[178:185], v[116:119]
	v_mfma_f32_16x16x128_f8f6f4 v[112:115], v[226:233], v[178:185], v[112:115]
	v_mfma_f32_16x16x128_f8f6f4 v[100:103], v[218:225], v[186:193], v[100:103]
	v_mfma_f32_16x16x128_f8f6f4 v[96:99], v[226:233], v[186:193], v[96:99]
	v_mfma_f32_16x16x128_f8f6f4 v[84:87], v[218:225], v[196:203], v[84:87]
	v_mfma_f32_16x16x128_f8f6f4 v[80:83], v[226:233], v[196:203], v[80:83]
	v_mfma_f32_16x16x128_f8f6f4 v[68:71], v[218:225], v[204:211], v[68:71]
	v_mfma_f32_16x16x128_f8f6f4 v[64:67], v[226:233], v[204:211], v[64:67]
	s_setprio 0
	s_barrier
	s_mov_b32 m0, s0
	ds_read_b128 v[178:181], v145 offset:16384
	ds_read_b128 v[186:189], v145 offset:18432
	ds_read_b128 v[182:185], v146 offset:16384
	ds_read_b128 v[190:193], v146 offset:18432
	ds_read_b128 v[196:199], v145 offset:20480
	ds_read_b128 v[204:207], v145 offset:22528
	ds_read_b128 v[200:203], v146 offset:20480
	ds_read_b128 v[208:211], v146 offset:22528
	global_load_lds_dwordx4 v132, s[46:47]
	s_mov_b32 m0, s56
	v_mov_b32_e32 v141, v133
	global_load_lds_dwordx4 v140, s[46:47]
	s_waitcnt lgkmcnt(8)
	s_barrier
	s_waitcnt lgkmcnt(0)
	v_lshl_add_u64 v[212:213], s[46:47], 0, v[132:133]
	v_lshl_add_u64 v[214:215], s[46:47], 0, v[140:141]
	s_setprio 1
	s_waitcnt lgkmcnt(0)
	v_mfma_f32_16x16x128_f8f6f4 v[60:63], v[162:169], v[178:185], v[60:63]
	v_mfma_f32_16x16x128_f8f6f4 v[56:59], v[170:177], v[178:185], v[56:59]
	v_mfma_f32_16x16x128_f8f6f4 v[44:47], v[162:169], v[186:193], v[44:47]
	v_mfma_f32_16x16x128_f8f6f4 v[40:43], v[170:177], v[186:193], v[40:43]
	v_mfma_f32_16x16x128_f8f6f4 v[28:31], v[162:169], v[196:203], v[28:31]
	v_mfma_f32_16x16x128_f8f6f4 v[24:27], v[170:177], v[196:203], v[24:27]
	v_mfma_f32_16x16x128_f8f6f4 v[12:15], v[162:169], v[204:211], v[12:15]
	v_mfma_f32_16x16x128_f8f6f4 v[8:11], v[170:177], v[204:211], v[8:11]
	s_setprio 0
	s_barrier
	s_mov_b32 m0, s1
	v_lshl_add_u64 v[140:141], s[50:51], 0, v[128:129]
	global_load_lds_dwordx4 v[140:141], off
	v_lshl_add_u64 v[142:143], s[50:51], 0, v[130:131]
	s_mov_b32 m0, s37
	s_nop 0
	global_load_lds_dwordx4 v[142:143], off
	s_waitcnt vmcnt(4)
	s_waitcnt lgkmcnt(0)
	s_barrier
	s_setprio 1
	s_waitcnt lgkmcnt(0)
	v_mfma_f32_16x16x128_f8f6f4 v[52:55], v[218:225], v[178:185], v[52:55]
	v_mfma_f32_16x16x128_f8f6f4 v[48:51], v[226:233], v[178:185], v[48:51]
	v_mfma_f32_16x16x128_f8f6f4 v[36:39], v[218:225], v[186:193], v[36:39]
	v_mfma_f32_16x16x128_f8f6f4 v[32:35], v[226:233], v[186:193], v[32:35]
	v_mfma_f32_16x16x128_f8f6f4 v[20:23], v[218:225], v[196:203], v[20:23]
	v_mfma_f32_16x16x128_f8f6f4 v[16:19], v[226:233], v[196:203], v[16:19]
	v_mfma_f32_16x16x128_f8f6f4 v[4:7], v[218:225], v[204:211], v[4:7]
	v_mfma_f32_16x16x128_f8f6f4 v[0:3], v[226:233], v[204:211], v[0:3]
	s_setprio 0
	s_barrier
	ds_read_b128 v[162:165], v147 offset:32768
	ds_read_b128 v[170:173], v147 offset:34816
	ds_read_b128 v[166:169], v148 offset:32768
	ds_read_b128 v[174:177], v148 offset:34816
	s_mov_b32 m0, s63
	ds_read_b128 v[178:181], v145 offset:32768
	ds_read_b128 v[186:189], v145 offset:34816
	ds_read_b128 v[182:185], v146 offset:32768
	ds_read_b128 v[190:193], v146 offset:34816
	ds_read_b128 v[196:199], v145 offset:36864
	ds_read_b128 v[204:207], v145 offset:38912
	ds_read_b128 v[200:203], v146 offset:36864
	ds_read_b128 v[208:211], v146 offset:38912
	v_cndmask_b32_e64 v132, v138, v160, s[42:43]
	global_load_lds_dwordx4 v161, s[46:47]
	s_mov_b32 m0, s64
	v_lshl_add_u64 v[216:217], s[48:49], 0, v[128:129]
	global_load_lds_dwordx4 v132, s[46:47]
	s_mov_b32 m0, s57
	s_nop 0
	global_load_lds_dwordx4 v[216:217], off
	v_lshl_add_u64 v[216:217], s[48:49], 0, v[130:131]
	s_mov_b32 m0, s62
	s_nop 0
	global_load_lds_dwordx4 v[216:217], off
	s_waitcnt lgkmcnt(8)
	s_barrier
	s_waitcnt lgkmcnt(0)
	s_setprio 1
	s_waitcnt lgkmcnt(0)
	v_mfma_f32_16x16x128_f8f6f4 v[124:127], v[162:169], v[178:185], v[124:127]
	v_mfma_f32_16x16x128_f8f6f4 v[120:123], v[170:177], v[178:185], v[120:123]
	v_mfma_f32_16x16x128_f8f6f4 v[108:111], v[162:169], v[186:193], v[108:111]
	v_mfma_f32_16x16x128_f8f6f4 v[104:107], v[170:177], v[186:193], v[104:107]
	v_mfma_f32_16x16x128_f8f6f4 v[92:95], v[162:169], v[196:203], v[92:95]
	v_mfma_f32_16x16x128_f8f6f4 v[88:91], v[170:177], v[196:203], v[88:91]
	v_mfma_f32_16x16x128_f8f6f4 v[76:79], v[162:169], v[204:211], v[76:79]
	v_mfma_f32_16x16x128_f8f6f4 v[72:75], v[170:177], v[204:211], v[72:75]
	s_setprio 0
	s_barrier
	ds_read_b128 v[218:221], v147 offset:49152
	ds_read_b128 v[226:229], v147 offset:51200
	ds_read_b128 v[222:225], v148 offset:49152
	ds_read_b128 v[230:233], v148 offset:51200
	s_barrier
	s_waitcnt lgkmcnt(0)
	s_setprio 1
	s_waitcnt lgkmcnt(0)
	v_mfma_f32_16x16x128_f8f6f4 v[116:119], v[218:225], v[178:185], v[116:119]
	v_mfma_f32_16x16x128_f8f6f4 v[112:115], v[226:233], v[178:185], v[112:115]
	v_mfma_f32_16x16x128_f8f6f4 v[100:103], v[218:225], v[186:193], v[100:103]
	v_mfma_f32_16x16x128_f8f6f4 v[96:99], v[226:233], v[186:193], v[96:99]
	v_mfma_f32_16x16x128_f8f6f4 v[84:87], v[218:225], v[196:203], v[84:87]
	v_mfma_f32_16x16x128_f8f6f4 v[80:83], v[226:233], v[196:203], v[80:83]
	v_mfma_f32_16x16x128_f8f6f4 v[68:71], v[218:225], v[204:211], v[68:71]
	v_mfma_f32_16x16x128_f8f6f4 v[64:67], v[226:233], v[204:211], v[64:67]
	s_setprio 0
	s_barrier
	s_mov_b32 m0, s67
	v_lshl_add_u64 v[212:213], v[212:213], 0, s[20:21]
	ds_read_b128 v[178:181], v145 offset:49152
	ds_read_b128 v[186:189], v145 offset:51200
	ds_read_b128 v[182:185], v146 offset:49152
	ds_read_b128 v[190:193], v146 offset:51200
	ds_read_b128 v[196:199], v145 offset:53248
	ds_read_b128 v[204:207], v145 offset:55296
	ds_read_b128 v[200:203], v146 offset:53248
	ds_read_b128 v[208:211], v146 offset:55296
	global_load_lds_dwordx4 v[212:213], off
	v_lshl_add_u64 v[212:213], v[214:215], 0, s[20:21]
	s_mov_b32 m0, s68
	s_nop 0
	global_load_lds_dwordx4 v[212:213], off
	s_waitcnt lgkmcnt(8)
	s_barrier
	s_waitcnt lgkmcnt(0)
	s_setprio 1
	s_waitcnt lgkmcnt(0)
	v_mfma_f32_16x16x128_f8f6f4 v[60:63], v[162:169], v[178:185], v[60:63]
	v_mfma_f32_16x16x128_f8f6f4 v[56:59], v[170:177], v[178:185], v[56:59]
	v_mfma_f32_16x16x128_f8f6f4 v[44:47], v[162:169], v[186:193], v[44:47]
	v_mfma_f32_16x16x128_f8f6f4 v[40:43], v[170:177], v[186:193], v[40:43]
	v_mfma_f32_16x16x128_f8f6f4 v[28:31], v[162:169], v[196:203], v[28:31]
	v_mfma_f32_16x16x128_f8f6f4 v[24:27], v[170:177], v[196:203], v[24:27]
	v_mfma_f32_16x16x128_f8f6f4 v[12:15], v[162:169], v[204:211], v[12:15]
	v_mfma_f32_16x16x128_f8f6f4 v[8:11], v[170:177], v[204:211], v[8:11]
	s_setprio 0
	s_barrier
	s_mov_b32 m0, s65
	v_lshl_add_u64 v[140:141], v[140:141], 0, s[20:21]
	global_load_lds_dwordx4 v[140:141], off
	v_lshl_add_u64 v[140:141], v[142:143], 0, s[20:21]
	s_mov_b32 m0, s66
	s_nop 0
	global_load_lds_dwordx4 v[140:141], off
	s_waitcnt vmcnt(4)
	s_waitcnt lgkmcnt(0)
	s_barrier
	s_setprio 1
	s_waitcnt lgkmcnt(0)
	v_mfma_f32_16x16x128_f8f6f4 v[52:55], v[218:225], v[178:185], v[52:55]
	v_mfma_f32_16x16x128_f8f6f4 v[48:51], v[226:233], v[178:185], v[48:51]
	v_mfma_f32_16x16x128_f8f6f4 v[36:39], v[218:225], v[186:193], v[36:39]
	v_mfma_f32_16x16x128_f8f6f4 v[32:35], v[226:233], v[186:193], v[32:35]
	v_mfma_f32_16x16x128_f8f6f4 v[20:23], v[218:225], v[196:203], v[20:23]
	v_mfma_f32_16x16x128_f8f6f4 v[16:19], v[226:233], v[196:203], v[16:19]
	v_mfma_f32_16x16x128_f8f6f4 v[4:7], v[218:225], v[204:211], v[4:7]
	v_mfma_f32_16x16x128_f8f6f4 v[0:3], v[226:233], v[204:211], v[0:3]
	s_setprio 0
	s_barrier
	s_mov_b32 m0, s69
	v_lshl_add_u64 v[140:141], s[44:45], 0, v[128:129]
	global_load_lds_dwordx4 v[140:141], off
	v_lshl_add_u64 v[140:141], s[44:45], 0, v[130:131]
	s_mov_b32 m0, s70
	s_andn2_b64 vcc, exec, s[40:41]
	global_load_lds_dwordx4 v[140:141], off
	s_mov_b64 s[42:43], -1
	s_mov_b64 s[40:41], 0
	s_mov_b64 s[44:45], 0x100
	s_cbranch_vccz .LBB0_1061

.LBB0_1080:
	v_mov_b32_e32 v137, v133
	v_mov_b32_e32 v139, v133
	s_mov_b64 s[34:35], 0
	s_mov_b64 s[28:29], -1
	s_mov_b64 s[30:31], 0
	s_add_u32 s42, s10, s34
	s_addc_u32 s43, s11, s35
	s_add_u32 s38, s42, 0x100
	s_addc_u32 s39, s43, 0
	s_and_b64 s[36:37], s[30:31], exec
	s_cselect_b32 s36, s10, s38
	s_cselect_b32 s37, s11, s39
	s_add_u32 s34, s26, s34
	s_addc_u32 s35, s27, s35
	s_add_u32 s38, s34, 0x100
	s_addc_u32 s39, s35, 0
	ds_read_b128 v[160:163], v147
	ds_read_b128 v[168:171], v147 offset:2048
	ds_read_b128 v[164:167], v148
	ds_read_b128 v[172:175], v148 offset:2048
	s_and_b64 s[34:35], s[30:31], exec
	s_cselect_b32 s41, s25, s39
	s_cselect_b32 s40, s24, s38
	s_add_i32 m0, s1, 0xc000
	s_add_i32 s64, s1, 0xe000
	s_add_u32 s38, s40, 0x1000
	s_addc_u32 s39, s41, 0
	s_add_u32 s34, s40, 0x1080
	s_addc_u32 s35, s41, 0
	v_cndmask_b32_e64 v132, v135, v155, s[30:31]
	v_cndmask_b32_e64 v159, v136, v157, s[30:31]
	v_lshl_add_u64 v[140:141], s[42:43], 0, v[136:137]
	v_lshl_add_u64 v[140:141], v[140:141], 0, s[16:17]
	ds_read_b128 v[176:179], v145
	ds_read_b128 v[184:187], v145 offset:2048
	ds_read_b128 v[180:183], v146
	ds_read_b128 v[188:191], v146 offset:2048
	ds_read_b128 v[196:199], v145 offset:4096
	ds_read_b128 v[204:207], v145 offset:6144
	ds_read_b128 v[200:203], v146 offset:4096
	ds_read_b128 v[208:211], v146 offset:6144
	global_load_lds_dwordx4 v[140:141], off
	v_lshl_add_u64 v[140:141], s[42:43], 0, v[138:139]
	v_lshl_add_u64 v[140:141], v[140:141], 0, s[16:17]
	s_mov_b32 m0, s64
	s_nop 0
	global_load_lds_dwordx4 v[140:141], off
	s_waitcnt lgkmcnt(8)
	s_barrier
	s_waitcnt lgkmcnt(0)
	v_cndmask_b32_e64 v140, v134, v156, s[30:31]
	s_setprio 1
	s_waitcnt lgkmcnt(0)
	v_mfma_f32_16x16x128_f8f6f4 v[124:127], v[160:167], v[176:183], 0
	v_mfma_f32_16x16x128_f8f6f4 v[120:123], v[168:175], v[176:183], 0
	v_mfma_f32_16x16x128_f8f6f4 v[108:111], v[160:167], v[184:191], 0
	v_mfma_f32_16x16x128_f8f6f4 v[104:107], v[168:175], v[184:191], 0
	v_mfma_f32_16x16x128_f8f6f4 v[92:95], v[160:167], v[196:203], 0
	v_mfma_f32_16x16x128_f8f6f4 v[88:91], v[168:175], v[196:203], 0
	v_mfma_f32_16x16x128_f8f6f4 v[76:79], v[160:167], v[204:211], 0
	v_mfma_f32_16x16x128_f8f6f4 v[72:75], v[168:175], v[204:211], 0
	s_setprio 0
	s_barrier
	ds_read_b128 v[218:221], v147 offset:16384
	ds_read_b128 v[226:229], v147 offset:18432
	ds_read_b128 v[222:225], v148 offset:16384
	ds_read_b128 v[230:233], v148 offset:18432
	s_barrier
	s_waitcnt lgkmcnt(0)
	s_setprio 1
	s_waitcnt lgkmcnt(0)
	v_mfma_f32_16x16x128_f8f6f4 v[116:119], v[218:225], v[176:183], 0
	v_mfma_f32_16x16x128_f8f6f4 v[112:115], v[226:233], v[176:183], 0
	v_mfma_f32_16x16x128_f8f6f4 v[100:103], v[218:225], v[184:191], 0
	v_mfma_f32_16x16x128_f8f6f4 v[96:99], v[226:233], v[184:191], 0
	v_mfma_f32_16x16x128_f8f6f4 v[84:87], v[218:225], v[196:203], 0
	v_mfma_f32_16x16x128_f8f6f4 v[80:83], v[226:233], v[196:203], 0
	v_mfma_f32_16x16x128_f8f6f4 v[68:71], v[218:225], v[204:211], 0
	v_mfma_f32_16x16x128_f8f6f4 v[64:67], v[226:233], v[204:211], 0
	s_setprio 0
	s_barrier
	s_mov_b32 m0, s1
	ds_read_b128 v[176:179], v145 offset:16384
	ds_read_b128 v[184:187], v145 offset:18432
	ds_read_b128 v[180:183], v146 offset:16384
	ds_read_b128 v[188:191], v146 offset:18432
	ds_read_b128 v[196:199], v145 offset:20480
	ds_read_b128 v[204:207], v145 offset:22528
	ds_read_b128 v[200:203], v146 offset:20480
	ds_read_b128 v[208:211], v146 offset:22528
	global_load_lds_dwordx4 v132, s[36:37]
	s_mov_b32 m0, s48
	v_mov_b32_e32 v141, v133
	global_load_lds_dwordx4 v140, s[36:37]
	s_waitcnt lgkmcnt(8)
	s_barrier
	s_waitcnt lgkmcnt(0)
	v_lshl_add_u64 v[192:193], s[36:37], 0, v[132:133]
	v_lshl_add_u64 v[212:213], s[36:37], 0, v[140:141]
	s_setprio 1
	s_waitcnt lgkmcnt(0)
	v_mfma_f32_16x16x128_f8f6f4 v[60:63], v[160:167], v[176:183], 0
	v_mfma_f32_16x16x128_f8f6f4 v[56:59], v[168:175], v[176:183], 0
	v_mfma_f32_16x16x128_f8f6f4 v[44:47], v[160:167], v[184:191], 0
	v_mfma_f32_16x16x128_f8f6f4 v[40:43], v[168:175], v[184:191], 0
	v_mfma_f32_16x16x128_f8f6f4 v[28:31], v[160:167], v[196:203], 0
	v_mfma_f32_16x16x128_f8f6f4 v[24:27], v[168:175], v[196:203], 0
	v_mfma_f32_16x16x128_f8f6f4 v[12:15], v[160:167], v[204:211], 0
	v_mfma_f32_16x16x128_f8f6f4 v[8:11], v[168:175], v[204:211], 0
	s_setprio 0
	s_barrier
	s_mov_b32 m0, s46
	v_lshl_add_u64 v[140:141], s[40:41], 0, v[130:131]
	global_load_lds_dwordx4 v[140:141], off
	v_lshl_add_u64 v[142:143], s[40:41], 0, v[128:129]
	s_mov_b32 m0, s47
	s_nop 0
	global_load_lds_dwordx4 v[142:143], off
	s_waitcnt vmcnt(4)
	s_waitcnt lgkmcnt(0)
	s_barrier
	s_setprio 1
	s_waitcnt lgkmcnt(0)
	v_mfma_f32_16x16x128_f8f6f4 v[52:55], v[218:225], v[176:183], 0
	v_mfma_f32_16x16x128_f8f6f4 v[48:51], v[226:233], v[176:183], 0
	v_mfma_f32_16x16x128_f8f6f4 v[36:39], v[218:225], v[184:191], 0
	v_mfma_f32_16x16x128_f8f6f4 v[32:35], v[226:233], v[184:191], 0
	v_mfma_f32_16x16x128_f8f6f4 v[20:23], v[218:225], v[196:203], 0
	v_mfma_f32_16x16x128_f8f6f4 v[16:19], v[226:233], v[196:203], 0
	v_mfma_f32_16x16x128_f8f6f4 v[4:7], v[218:225], v[204:211], 0
	v_mfma_f32_16x16x128_f8f6f4 v[0:3], v[226:233], v[204:211], 0
	s_setprio 0
	s_barrier
	ds_read_b128 v[160:163], v147 offset:32768
	ds_read_b128 v[168:171], v147 offset:34816
	ds_read_b128 v[164:167], v148 offset:32768
	ds_read_b128 v[172:175], v148 offset:34816
	s_mov_b32 m0, s51
	ds_read_b128 v[176:179], v145 offset:32768
	ds_read_b128 v[184:187], v145 offset:34816
	ds_read_b128 v[180:183], v146 offset:32768
	ds_read_b128 v[188:191], v146 offset:34816
	ds_read_b128 v[196:199], v145 offset:36864
	ds_read_b128 v[204:207], v145 offset:38912
	ds_read_b128 v[200:203], v146 offset:36864
	ds_read_b128 v[208:211], v146 offset:38912
	v_cndmask_b32_e64 v132, v138, v158, s[30:31]
	global_load_lds_dwordx4 v159, s[36:37]
	s_mov_b32 m0, s52
	v_lshl_add_u64 v[214:215], s[38:39], 0, v[130:131]
	global_load_lds_dwordx4 v132, s[36:37]
	s_mov_b32 m0, s49
	s_nop 0
	global_load_lds_dwordx4 v[214:215], off
	v_lshl_add_u64 v[214:215], s[38:39], 0, v[128:129]
	s_mov_b32 m0, s50
	s_nop 0
	global_load_lds_dwordx4 v[214:215], off
	s_waitcnt lgkmcnt(8)
	s_barrier
	s_waitcnt lgkmcnt(0)
	s_setprio 1
	s_waitcnt lgkmcnt(0)
	v_mfma_f32_16x16x128_f8f6f4 v[124:127], v[160:167], v[176:183], v[124:127]
	v_mfma_f32_16x16x128_f8f6f4 v[120:123], v[168:175], v[176:183], v[120:123]
	v_mfma_f32_16x16x128_f8f6f4 v[108:111], v[160:167], v[184:191], v[108:111]
	v_mfma_f32_16x16x128_f8f6f4 v[104:107], v[168:175], v[184:191], v[104:107]
	v_mfma_f32_16x16x128_f8f6f4 v[92:95], v[160:167], v[196:203], v[92:95]
	v_mfma_f32_16x16x128_f8f6f4 v[88:91], v[168:175], v[196:203], v[88:91]
	v_mfma_f32_16x16x128_f8f6f4 v[76:79], v[160:167], v[204:211], v[76:79]
	v_mfma_f32_16x16x128_f8f6f4 v[72:75], v[168:175], v[204:211], v[72:75]
	s_setprio 0
	s_barrier
	ds_read_b128 v[218:221], v147 offset:49152
	ds_read_b128 v[226:229], v147 offset:51200
	ds_read_b128 v[222:225], v148 offset:49152
	ds_read_b128 v[230:233], v148 offset:51200
	s_barrier
	s_waitcnt lgkmcnt(0)
	s_setprio 1
	s_waitcnt lgkmcnt(0)
	v_mfma_f32_16x16x128_f8f6f4 v[116:119], v[218:225], v[176:183], v[116:119]
	v_mfma_f32_16x16x128_f8f6f4 v[112:115], v[226:233], v[176:183], v[112:115]
	v_mfma_f32_16x16x128_f8f6f4 v[100:103], v[218:225], v[184:191], v[100:103]
	v_mfma_f32_16x16x128_f8f6f4 v[96:99], v[226:233], v[184:191], v[96:99]
	v_mfma_f32_16x16x128_f8f6f4 v[84:87], v[218:225], v[196:203], v[84:87]
	v_mfma_f32_16x16x128_f8f6f4 v[80:83], v[226:233], v[196:203], v[80:83]
	v_mfma_f32_16x16x128_f8f6f4 v[68:71], v[218:225], v[204:211], v[68:71]
	v_mfma_f32_16x16x128_f8f6f4 v[64:67], v[226:233], v[204:211], v[64:67]
	s_setprio 0
	s_barrier
	s_mov_b32 m0, s56
	v_lshl_add_u64 v[192:193], v[192:193], 0, s[16:17]
	ds_read_b128 v[176:179], v145 offset:49152
	ds_read_b128 v[184:187], v145 offset:51200
	ds_read_b128 v[180:183], v146 offset:49152
	ds_read_b128 v[188:191], v146 offset:51200
	ds_read_b128 v[196:199], v145 offset:53248
	ds_read_b128 v[204:207], v145 offset:55296
	ds_read_b128 v[200:203], v146 offset:53248
	ds_read_b128 v[208:211], v146 offset:55296
	global_load_lds_dwordx4 v[192:193], off
	v_lshl_add_u64 v[192:193], v[212:213], 0, s[16:17]
	s_mov_b32 m0, s57
	s_nop 0
	global_load_lds_dwordx4 v[192:193], off
	s_waitcnt lgkmcnt(8)
	s_barrier
	s_waitcnt lgkmcnt(0)
	s_setprio 1
	s_waitcnt lgkmcnt(0)
	v_mfma_f32_16x16x128_f8f6f4 v[60:63], v[160:167], v[176:183], v[60:63]
	v_mfma_f32_16x16x128_f8f6f4 v[56:59], v[168:175], v[176:183], v[56:59]
	v_mfma_f32_16x16x128_f8f6f4 v[44:47], v[160:167], v[184:191], v[44:47]
	v_mfma_f32_16x16x128_f8f6f4 v[40:43], v[168:175], v[184:191], v[40:43]
	v_mfma_f32_16x16x128_f8f6f4 v[28:31], v[160:167], v[196:203], v[28:31]
	v_mfma_f32_16x16x128_f8f6f4 v[24:27], v[168:175], v[196:203], v[24:27]
	v_mfma_f32_16x16x128_f8f6f4 v[12:15], v[160:167], v[204:211], v[12:15]
	v_mfma_f32_16x16x128_f8f6f4 v[8:11], v[168:175], v[204:211], v[8:11]
	s_setprio 0
	s_barrier
	s_mov_b32 m0, s54
	v_lshl_add_u64 v[140:141], v[140:141], 0, s[16:17]
	global_load_lds_dwordx4 v[140:141], off
	v_lshl_add_u64 v[140:141], v[142:143], 0, s[16:17]
	s_mov_b32 m0, s55
	s_nop 0
	global_load_lds_dwordx4 v[140:141], off
	s_waitcnt vmcnt(4)
	s_waitcnt lgkmcnt(0)
	s_barrier
	s_setprio 1
	s_waitcnt lgkmcnt(0)
	v_mfma_f32_16x16x128_f8f6f4 v[52:55], v[218:225], v[176:183], v[52:55]
	v_mfma_f32_16x16x128_f8f6f4 v[48:51], v[226:233], v[176:183], v[48:51]
	v_mfma_f32_16x16x128_f8f6f4 v[36:39], v[218:225], v[184:191], v[36:39]
	v_mfma_f32_16x16x128_f8f6f4 v[32:35], v[226:233], v[184:191], v[32:35]
	v_mfma_f32_16x16x128_f8f6f4 v[20:23], v[218:225], v[196:203], v[20:23]
	v_mfma_f32_16x16x128_f8f6f4 v[16:19], v[226:233], v[196:203], v[16:19]
	v_mfma_f32_16x16x128_f8f6f4 v[4:7], v[218:225], v[204:211], v[4:7]
	v_mfma_f32_16x16x128_f8f6f4 v[0:3], v[226:233], v[204:211], v[0:3]
	s_setprio 0
	s_barrier
	s_mov_b32 m0, s58
	v_lshl_add_u64 v[140:141], s[34:35], 0, v[130:131]
	global_load_lds_dwordx4 v[140:141], off
	v_lshl_add_u64 v[140:141], s[34:35], 0, v[128:129]
	s_mov_b32 m0, s59
	s_andn2_b64 vcc, exec, s[28:29]
	global_load_lds_dwordx4 v[140:141], off
	s_mov_b64 s[30:31], -1
	s_mov_b64 s[28:29], 0
	s_mov_b64 s[34:35], 0x100
	s_cbranch_vccz .LBB0_1081
	s_branch .Lpeel_after_1081
.LBB0_1081:
	s_add_u32 s42, s10, s34
	s_addc_u32 s43, s11, s35
	s_add_u32 s38, s42, 0x100
	s_addc_u32 s39, s43, 0
	s_and_b64 s[36:37], s[30:31], exec
	s_cselect_b32 s36, s10, s38
	s_cselect_b32 s37, s11, s39
	s_add_u32 s34, s26, s34
	s_addc_u32 s35, s27, s35
	s_add_u32 s38, s34, 0x100
	s_addc_u32 s39, s35, 0
	ds_read_b128 v[160:163], v147
	ds_read_b128 v[168:171], v147 offset:2048
	ds_read_b128 v[164:167], v148
	ds_read_b128 v[172:175], v148 offset:2048
	s_and_b64 s[34:35], s[30:31], exec
	s_cselect_b32 s41, s25, s39
	s_cselect_b32 s40, s24, s38
	s_add_i32 m0, s1, 0xc000
	s_add_i32 s64, s1, 0xe000
	s_add_u32 s38, s40, 0x1000
	s_addc_u32 s39, s41, 0
	s_add_u32 s34, s40, 0x1080
	s_addc_u32 s35, s41, 0
	v_cndmask_b32_e64 v132, v135, v155, s[30:31]
	v_cndmask_b32_e64 v159, v136, v157, s[30:31]
	v_lshl_add_u64 v[140:141], s[42:43], 0, v[136:137]
	v_lshl_add_u64 v[140:141], v[140:141], 0, s[16:17]
	ds_read_b128 v[176:179], v145
	ds_read_b128 v[184:187], v145 offset:2048
	ds_read_b128 v[180:183], v146
	ds_read_b128 v[188:191], v146 offset:2048
	ds_read_b128 v[196:199], v145 offset:4096
	ds_read_b128 v[204:207], v145 offset:6144
	ds_read_b128 v[200:203], v146 offset:4096
	ds_read_b128 v[208:211], v146 offset:6144
	global_load_lds_dwordx4 v[140:141], off
	v_lshl_add_u64 v[140:141], s[42:43], 0, v[138:139]
	v_lshl_add_u64 v[140:141], v[140:141], 0, s[16:17]
	s_mov_b32 m0, s64
	s_nop 0
	global_load_lds_dwordx4 v[140:141], off
	s_waitcnt lgkmcnt(8)
	s_barrier
	s_waitcnt lgkmcnt(0)
	v_cndmask_b32_e64 v140, v134, v156, s[30:31]
	s_setprio 1
	s_waitcnt lgkmcnt(0)
	v_mfma_f32_16x16x128_f8f6f4 v[124:127], v[160:167], v[176:183], v[124:127]
	v_mfma_f32_16x16x128_f8f6f4 v[120:123], v[168:175], v[176:183], v[120:123]
	v_mfma_f32_16x16x128_f8f6f4 v[108:111], v[160:167], v[184:191], v[108:111]
	v_mfma_f32_16x16x128_f8f6f4 v[104:107], v[168:175], v[184:191], v[104:107]
	v_mfma_f32_16x16x128_f8f6f4 v[92:95], v[160:167], v[196:203], v[92:95]
	v_mfma_f32_16x16x128_f8f6f4 v[88:91], v[168:175], v[196:203], v[88:91]
	v_mfma_f32_16x16x128_f8f6f4 v[76:79], v[160:167], v[204:211], v[76:79]
	v_mfma_f32_16x16x128_f8f6f4 v[72:75], v[168:175], v[204:211], v[72:75]
	s_setprio 0
	s_barrier
	ds_read_b128 v[218:221], v147 offset:16384
	ds_read_b128 v[226:229], v147 offset:18432
	ds_read_b128 v[222:225], v148 offset:16384
	ds_read_b128 v[230:233], v148 offset:18432
	s_barrier
	s_waitcnt lgkmcnt(0)
	s_setprio 1
	s_waitcnt lgkmcnt(0)
	v_mfma_f32_16x16x128_f8f6f4 v[116:119], v[218:225], v[176:183], v[116:119]
	v_mfma_f32_16x16x128_f8f6f4 v[112:115], v[226:233], v[176:183], v[112:115]
	v_mfma_f32_16x16x128_f8f6f4 v[100:103], v[218:225], v[184:191], v[100:103]
	v_mfma_f32_16x16x128_f8f6f4 v[96:99], v[226:233], v[184:191], v[96:99]
	v_mfma_f32_16x16x128_f8f6f4 v[84:87], v[218:225], v[196:203], v[84:87]
	v_mfma_f32_16x16x128_f8f6f4 v[80:83], v[226:233], v[196:203], v[80:83]
	v_mfma_f32_16x16x128_f8f6f4 v[68:71], v[218:225], v[204:211], v[68:71]
	v_mfma_f32_16x16x128_f8f6f4 v[64:67], v[226:233], v[204:211], v[64:67]
	s_setprio 0
	s_barrier
	s_mov_b32 m0, s1
	ds_read_b128 v[176:179], v145 offset:16384
	ds_read_b128 v[184:187], v145 offset:18432
	ds_read_b128 v[180:183], v146 offset:16384
	ds_read_b128 v[188:191], v146 offset:18432
	ds_read_b128 v[196:199], v145 offset:20480
	ds_read_b128 v[204:207], v145 offset:22528
	ds_read_b128 v[200:203], v146 offset:20480
	ds_read_b128 v[208:211], v146 offset:22528
	global_load_lds_dwordx4 v132, s[36:37]
	s_mov_b32 m0, s48
	v_mov_b32_e32 v141, v133
	global_load_lds_dwordx4 v140, s[36:37]
	s_waitcnt lgkmcnt(8)
	s_barrier
	s_waitcnt lgkmcnt(0)
	v_lshl_add_u64 v[192:193], s[36:37], 0, v[132:133]
	v_lshl_add_u64 v[212:213], s[36:37], 0, v[140:141]
	s_setprio 1
	s_waitcnt lgkmcnt(0)
	v_mfma_f32_16x16x128_f8f6f4 v[60:63], v[160:167], v[176:183], v[60:63]
	v_mfma_f32_16x16x128_f8f6f4 v[56:59], v[168:175], v[176:183], v[56:59]
	v_mfma_f32_16x16x128_f8f6f4 v[44:47], v[160:167], v[184:191], v[44:47]
	v_mfma_f32_16x16x128_f8f6f4 v[40:43], v[168:175], v[184:191], v[40:43]
	v_mfma_f32_16x16x128_f8f6f4 v[28:31], v[160:167], v[196:203], v[28:31]
	v_mfma_f32_16x16x128_f8f6f4 v[24:27], v[168:175], v[196:203], v[24:27]
	v_mfma_f32_16x16x128_f8f6f4 v[12:15], v[160:167], v[204:211], v[12:15]
	v_mfma_f32_16x16x128_f8f6f4 v[8:11], v[168:175], v[204:211], v[8:11]
	s_setprio 0
	s_barrier
	s_mov_b32 m0, s46
	v_lshl_add_u64 v[140:141], s[40:41], 0, v[130:131]
	global_load_lds_dwordx4 v[140:141], off
	v_lshl_add_u64 v[142:143], s[40:41], 0, v[128:129]
	s_mov_b32 m0, s47
	s_nop 0
	global_load_lds_dwordx4 v[142:143], off
	s_waitcnt vmcnt(4)
	s_waitcnt lgkmcnt(0)
	s_barrier
	s_setprio 1
	s_waitcnt lgkmcnt(0)
	v_mfma_f32_16x16x128_f8f6f4 v[52:55], v[218:225], v[176:183], v[52:55]
	v_mfma_f32_16x16x128_f8f6f4 v[48:51], v[226:233], v[176:183], v[48:51]
	v_mfma_f32_16x16x128_f8f6f4 v[36:39], v[218:225], v[184:191], v[36:39]
	v_mfma_f32_16x16x128_f8f6f4 v[32:35], v[226:233], v[184:191], v[32:35]
	v_mfma_f32_16x16x128_f8f6f4 v[20:23], v[218:225], v[196:203], v[20:23]
	v_mfma_f32_16x16x128_f8f6f4 v[16:19], v[226:233], v[196:203], v[16:19]
	v_mfma_f32_16x16x128_f8f6f4 v[4:7], v[218:225], v[204:211], v[4:7]
	v_mfma_f32_16x16x128_f8f6f4 v[0:3], v[226:233], v[204:211], v[0:3]
	s_setprio 0
	s_barrier
	ds_read_b128 v[160:163], v147 offset:32768
	ds_read_b128 v[168:171], v147 offset:34816
	ds_read_b128 v[164:167], v148 offset:32768
	ds_read_b128 v[172:175], v148 offset:34816
	s_mov_b32 m0, s51
	ds_read_b128 v[176:179], v145 offset:32768
	ds_read_b128 v[184:187], v145 offset:34816
	ds_read_b128 v[180:183], v146 offset:32768
	ds_read_b128 v[188:191], v146 offset:34816
	ds_read_b128 v[196:199], v145 offset:36864
	ds_read_b128 v[204:207], v145 offset:38912
	ds_read_b128 v[200:203], v146 offset:36864
	ds_read_b128 v[208:211], v146 offset:38912
	v_cndmask_b32_e64 v132, v138, v158, s[30:31]
	global_load_lds_dwordx4 v159, s[36:37]
	s_mov_b32 m0, s52
	v_lshl_add_u64 v[214:215], s[38:39], 0, v[130:131]
	global_load_lds_dwordx4 v132, s[36:37]
	s_mov_b32 m0, s49
	s_nop 0
	global_load_lds_dwordx4 v[214:215], off
	v_lshl_add_u64 v[214:215], s[38:39], 0, v[128:129]
	s_mov_b32 m0, s50
	s_nop 0
	global_load_lds_dwordx4 v[214:215], off
	s_waitcnt lgkmcnt(8)
	s_barrier
	s_waitcnt lgkmcnt(0)
	s_setprio 1
	s_waitcnt lgkmcnt(0)
	v_mfma_f32_16x16x128_f8f6f4 v[124:127], v[160:167], v[176:183], v[124:127]
	v_mfma_f32_16x16x128_f8f6f4 v[120:123], v[168:175], v[176:183], v[120:123]
	v_mfma_f32_16x16x128_f8f6f4 v[108:111], v[160:167], v[184:191], v[108:111]
	v_mfma_f32_16x16x128_f8f6f4 v[104:107], v[168:175], v[184:191], v[104:107]
	v_mfma_f32_16x16x128_f8f6f4 v[92:95], v[160:167], v[196:203], v[92:95]
	v_mfma_f32_16x16x128_f8f6f4 v[88:91], v[168:175], v[196:203], v[88:91]
	v_mfma_f32_16x16x128_f8f6f4 v[76:79], v[160:167], v[204:211], v[76:79]
	v_mfma_f32_16x16x128_f8f6f4 v[72:75], v[168:175], v[204:211], v[72:75]
	s_setprio 0
	s_barrier
	ds_read_b128 v[218:221], v147 offset:49152
	ds_read_b128 v[226:229], v147 offset:51200
	ds_read_b128 v[222:225], v148 offset:49152
	ds_read_b128 v[230:233], v148 offset:51200
	s_barrier
	s_waitcnt lgkmcnt(0)
	s_setprio 1
	s_waitcnt lgkmcnt(0)
	v_mfma_f32_16x16x128_f8f6f4 v[116:119], v[218:225], v[176:183], v[116:119]
	v_mfma_f32_16x16x128_f8f6f4 v[112:115], v[226:233], v[176:183], v[112:115]
	v_mfma_f32_16x16x128_f8f6f4 v[100:103], v[218:225], v[184:191], v[100:103]
	v_mfma_f32_16x16x128_f8f6f4 v[96:99], v[226:233], v[184:191], v[96:99]
	v_mfma_f32_16x16x128_f8f6f4 v[84:87], v[218:225], v[196:203], v[84:87]
	v_mfma_f32_16x16x128_f8f6f4 v[80:83], v[226:233], v[196:203], v[80:83]
	v_mfma_f32_16x16x128_f8f6f4 v[68:71], v[218:225], v[204:211], v[68:71]
	v_mfma_f32_16x16x128_f8f6f4 v[64:67], v[226:233], v[204:211], v[64:67]
	s_setprio 0
	s_barrier
	s_mov_b32 m0, s56
	v_lshl_add_u64 v[192:193], v[192:193], 0, s[16:17]
	ds_read_b128 v[176:179], v145 offset:49152
	ds_read_b128 v[184:187], v145 offset:51200
	ds_read_b128 v[180:183], v146 offset:49152
	ds_read_b128 v[188:191], v146 offset:51200
	ds_read_b128 v[196:199], v145 offset:53248
	ds_read_b128 v[204:207], v145 offset:55296
	ds_read_b128 v[200:203], v146 offset:53248
	ds_read_b128 v[208:211], v146 offset:55296
	global_load_lds_dwordx4 v[192:193], off
	v_lshl_add_u64 v[192:193], v[212:213], 0, s[16:17]
	s_mov_b32 m0, s57
	s_nop 0
	global_load_lds_dwordx4 v[192:193], off
	s_waitcnt lgkmcnt(8)
	s_barrier
	s_waitcnt lgkmcnt(0)
	s_setprio 1
	s_waitcnt lgkmcnt(0)
	v_mfma_f32_16x16x128_f8f6f4 v[60:63], v[160:167], v[176:183], v[60:63]
	v_mfma_f32_16x16x128_f8f6f4 v[56:59], v[168:175], v[176:183], v[56:59]
	v_mfma_f32_16x16x128_f8f6f4 v[44:47], v[160:167], v[184:191], v[44:47]
	v_mfma_f32_16x16x128_f8f6f4 v[40:43], v[168:175], v[184:191], v[40:43]
	v_mfma_f32_16x16x128_f8f6f4 v[28:31], v[160:167], v[196:203], v[28:31]
	v_mfma_f32_16x16x128_f8f6f4 v[24:27], v[168:175], v[196:203], v[24:27]
	v_mfma_f32_16x16x128_f8f6f4 v[12:15], v[160:167], v[204:211], v[12:15]
	v_mfma_f32_16x16x128_f8f6f4 v[8:11], v[168:175], v[204:211], v[8:11]
	s_setprio 0
	s_barrier
	s_mov_b32 m0, s54
	v_lshl_add_u64 v[140:141], v[140:141], 0, s[16:17]
	global_load_lds_dwordx4 v[140:141], off
	v_lshl_add_u64 v[140:141], v[142:143], 0, s[16:17]
	s_mov_b32 m0, s55
	s_nop 0
	global_load_lds_dwordx4 v[140:141], off
	s_waitcnt vmcnt(4)
	s_waitcnt lgkmcnt(0)
	s_barrier
	s_setprio 1
	s_waitcnt lgkmcnt(0)
	v_mfma_f32_16x16x128_f8f6f4 v[52:55], v[218:225], v[176:183], v[52:55]
	v_mfma_f32_16x16x128_f8f6f4 v[48:51], v[226:233], v[176:183], v[48:51]
	v_mfma_f32_16x16x128_f8f6f4 v[36:39], v[218:225], v[184:191], v[36:39]
	v_mfma_f32_16x16x128_f8f6f4 v[32:35], v[226:233], v[184:191], v[32:35]
	v_mfma_f32_16x16x128_f8f6f4 v[20:23], v[218:225], v[196:203], v[20:23]
	v_mfma_f32_16x16x128_f8f6f4 v[16:19], v[226:233], v[196:203], v[16:19]
	v_mfma_f32_16x16x128_f8f6f4 v[4:7], v[218:225], v[204:211], v[4:7]
	v_mfma_f32_16x16x128_f8f6f4 v[0:3], v[226:233], v[204:211], v[0:3]
	s_setprio 0
	s_barrier
	s_mov_b32 m0, s58
	v_lshl_add_u64 v[140:141], s[34:35], 0, v[130:131]
	global_load_lds_dwordx4 v[140:141], off
	v_lshl_add_u64 v[140:141], s[34:35], 0, v[128:129]
	s_mov_b32 m0, s59
	s_andn2_b64 vcc, exec, s[28:29]
	global_load_lds_dwordx4 v[140:141], off
	s_mov_b64 s[30:31], -1
	s_mov_b64 s[28:29], 0
	s_mov_b64 s[34:35], 0x100
	s_cbranch_vccz .LBB0_1081

.LBB0_1960:
	v_mov_b32_e32 v137, v133
	v_mov_b32_e32 v139, v133
	s_mov_b64 s[44:45], 0
	s_mov_b64 s[40:41], -1
	s_mov_b64 s[42:43], 0
	s_add_u32 s52, s12, s44
	s_addc_u32 s53, s13, s45
	s_add_u32 s29, s52, 0x100
	s_addc_u32 s48, s53, 0
	s_and_b64 s[46:47], s[42:43], exec
	s_cselect_b32 s46, s12, s29
	s_cselect_b32 s47, s13, s48
	s_add_u32 s29, s38, s44
	s_addc_u32 s44, s39, s45
	s_add_u32 s29, s29, 0x100
	s_addc_u32 s48, s44, 0
	ds_read_b128 v[162:165], v147
	ds_read_b128 v[170:173], v147 offset:2048
	ds_read_b128 v[166:169], v148
	ds_read_b128 v[174:177], v148 offset:2048
	s_and_b64 s[44:45], s[42:43], exec
	s_cselect_b32 s51, s35, s48
	s_cselect_b32 s50, s34, s29
	s_add_i32 m0, s0, 0xc000
	s_add_i32 s29, s0, 0xe000
	s_add_u32 s48, s50, 0x1000
	s_addc_u32 s49, s51, 0
	s_add_u32 s44, s50, 0x1080
	s_addc_u32 s45, s51, 0
	v_cndmask_b32_e64 v132, v135, v157, s[42:43]
	v_cndmask_b32_e64 v161, v136, v159, s[42:43]
	v_lshl_add_u64 v[140:141], s[52:53], 0, v[136:137]
	v_lshl_add_u64 v[140:141], v[140:141], 0, s[20:21]
	ds_read_b128 v[178:181], v145
	ds_read_b128 v[186:189], v145 offset:2048
	ds_read_b128 v[182:185], v146
	ds_read_b128 v[190:193], v146 offset:2048
	ds_read_b128 v[196:199], v145 offset:4096
	ds_read_b128 v[204:207], v145 offset:6144
	ds_read_b128 v[200:203], v146 offset:4096
	ds_read_b128 v[208:211], v146 offset:6144
	global_load_lds_dwordx4 v[140:141], off
	v_lshl_add_u64 v[140:141], s[52:53], 0, v[138:139]
	v_lshl_add_u64 v[140:141], v[140:141], 0, s[20:21]
	s_mov_b32 m0, s29
	s_nop 0
	global_load_lds_dwordx4 v[140:141], off
	s_waitcnt lgkmcnt(8)
	s_barrier
	s_waitcnt lgkmcnt(0)
	v_cndmask_b32_e64 v140, v134, v158, s[42:43]
	s_setprio 1
	s_waitcnt lgkmcnt(0)
	v_mfma_f32_16x16x128_f8f6f4 v[124:127], v[162:169], v[178:185], 0
	v_mfma_f32_16x16x128_f8f6f4 v[120:123], v[170:177], v[178:185], 0
	v_mfma_f32_16x16x128_f8f6f4 v[108:111], v[162:169], v[186:193], 0
	v_mfma_f32_16x16x128_f8f6f4 v[104:107], v[170:177], v[186:193], 0
	v_mfma_f32_16x16x128_f8f6f4 v[92:95], v[162:169], v[196:203], 0
	v_mfma_f32_16x16x128_f8f6f4 v[88:91], v[170:177], v[196:203], 0
	v_mfma_f32_16x16x128_f8f6f4 v[76:79], v[162:169], v[204:211], 0
	v_mfma_f32_16x16x128_f8f6f4 v[72:75], v[170:177], v[204:211], 0
	s_setprio 0
	s_barrier
	ds_read_b128 v[218:221], v147 offset:16384
	ds_read_b128 v[226:229], v147 offset:18432
	ds_read_b128 v[222:225], v148 offset:16384
	ds_read_b128 v[230:233], v148 offset:18432
	s_barrier
	s_waitcnt lgkmcnt(0)
	s_setprio 1
	s_waitcnt lgkmcnt(0)
	v_mfma_f32_16x16x128_f8f6f4 v[116:119], v[218:225], v[178:185], 0
	v_mfma_f32_16x16x128_f8f6f4 v[112:115], v[226:233], v[178:185], 0
	v_mfma_f32_16x16x128_f8f6f4 v[100:103], v[218:225], v[186:193], 0
	v_mfma_f32_16x16x128_f8f6f4 v[96:99], v[226:233], v[186:193], 0
	v_mfma_f32_16x16x128_f8f6f4 v[84:87], v[218:225], v[196:203], 0
	v_mfma_f32_16x16x128_f8f6f4 v[80:83], v[226:233], v[196:203], 0
	v_mfma_f32_16x16x128_f8f6f4 v[68:71], v[218:225], v[204:211], 0
	v_mfma_f32_16x16x128_f8f6f4 v[64:67], v[226:233], v[204:211], 0
	s_setprio 0
	s_barrier
	s_mov_b32 m0, s0
	ds_read_b128 v[178:181], v145 offset:16384
	ds_read_b128 v[186:189], v145 offset:18432
	ds_read_b128 v[182:185], v146 offset:16384
	ds_read_b128 v[190:193], v146 offset:18432
	ds_read_b128 v[196:199], v145 offset:20480
	ds_read_b128 v[204:207], v145 offset:22528
	ds_read_b128 v[200:203], v146 offset:20480
	ds_read_b128 v[208:211], v146 offset:22528
	global_load_lds_dwordx4 v132, s[46:47]
	s_mov_b32 m0, s56
	v_mov_b32_e32 v141, v133
	global_load_lds_dwordx4 v140, s[46:47]
	s_waitcnt lgkmcnt(8)
	s_barrier
	s_waitcnt lgkmcnt(0)
	v_lshl_add_u64 v[212:213], s[46:47], 0, v[132:133]
	v_lshl_add_u64 v[214:215], s[46:47], 0, v[140:141]
	s_setprio 1
	s_waitcnt lgkmcnt(0)
	v_mfma_f32_16x16x128_f8f6f4 v[60:63], v[162:169], v[178:185], 0
	v_mfma_f32_16x16x128_f8f6f4 v[56:59], v[170:177], v[178:185], 0
	v_mfma_f32_16x16x128_f8f6f4 v[44:47], v[162:169], v[186:193], 0
	v_mfma_f32_16x16x128_f8f6f4 v[40:43], v[170:177], v[186:193], 0
	v_mfma_f32_16x16x128_f8f6f4 v[28:31], v[162:169], v[196:203], 0
	v_mfma_f32_16x16x128_f8f6f4 v[24:27], v[170:177], v[196:203], 0
	v_mfma_f32_16x16x128_f8f6f4 v[12:15], v[162:169], v[204:211], 0
	v_mfma_f32_16x16x128_f8f6f4 v[8:11], v[170:177], v[204:211], 0
	s_setprio 0
	s_barrier
	s_mov_b32 m0, s1
	v_lshl_add_u64 v[140:141], s[50:51], 0, v[128:129]
	global_load_lds_dwordx4 v[140:141], off
	v_lshl_add_u64 v[142:143], s[50:51], 0, v[130:131]
	s_mov_b32 m0, s37
	s_nop 0
	global_load_lds_dwordx4 v[142:143], off
	s_waitcnt vmcnt(4)
	s_waitcnt lgkmcnt(0)
	s_barrier
	s_setprio 1
	s_waitcnt lgkmcnt(0)
	v_mfma_f32_16x16x128_f8f6f4 v[52:55], v[218:225], v[178:185], 0
	v_mfma_f32_16x16x128_f8f6f4 v[48:51], v[226:233], v[178:185], 0
	v_mfma_f32_16x16x128_f8f6f4 v[36:39], v[218:225], v[186:193], 0
	v_mfma_f32_16x16x128_f8f6f4 v[32:35], v[226:233], v[186:193], 0
	v_mfma_f32_16x16x128_f8f6f4 v[20:23], v[218:225], v[196:203], 0
	v_mfma_f32_16x16x128_f8f6f4 v[16:19], v[226:233], v[196:203], 0
	v_mfma_f32_16x16x128_f8f6f4 v[4:7], v[218:225], v[204:211], 0
	v_mfma_f32_16x16x128_f8f6f4 v[0:3], v[226:233], v[204:211], 0
	s_setprio 0
	s_barrier
	ds_read_b128 v[162:165], v147 offset:32768
	ds_read_b128 v[170:173], v147 offset:34816
	ds_read_b128 v[166:169], v148 offset:32768
	ds_read_b128 v[174:177], v148 offset:34816
	s_mov_b32 m0, s65
	ds_read_b128 v[178:181], v145 offset:32768
	ds_read_b128 v[186:189], v145 offset:34816
	ds_read_b128 v[182:185], v146 offset:32768
	ds_read_b128 v[190:193], v146 offset:34816
	ds_read_b128 v[196:199], v145 offset:36864
	ds_read_b128 v[204:207], v145 offset:38912
	ds_read_b128 v[200:203], v146 offset:36864
	ds_read_b128 v[208:211], v146 offset:38912
	v_cndmask_b32_e64 v132, v138, v160, s[42:43]
	global_load_lds_dwordx4 v161, s[46:47]
	s_mov_b32 m0, s66
	v_lshl_add_u64 v[216:217], s[48:49], 0, v[128:129]
	global_load_lds_dwordx4 v132, s[46:47]
	s_mov_b32 m0, s57
	s_nop 0
	global_load_lds_dwordx4 v[216:217], off
	v_lshl_add_u64 v[216:217], s[48:49], 0, v[130:131]
	s_mov_b32 m0, s64
	s_nop 0
	global_load_lds_dwordx4 v[216:217], off
	s_waitcnt lgkmcnt(8)
	s_barrier
	s_waitcnt lgkmcnt(0)
	s_setprio 1
	s_waitcnt lgkmcnt(0)
	v_mfma_f32_16x16x128_f8f6f4 v[124:127], v[162:169], v[178:185], v[124:127]
	v_mfma_f32_16x16x128_f8f6f4 v[120:123], v[170:177], v[178:185], v[120:123]
	v_mfma_f32_16x16x128_f8f6f4 v[108:111], v[162:169], v[186:193], v[108:111]
	v_mfma_f32_16x16x128_f8f6f4 v[104:107], v[170:177], v[186:193], v[104:107]
	v_mfma_f32_16x16x128_f8f6f4 v[92:95], v[162:169], v[196:203], v[92:95]
	v_mfma_f32_16x16x128_f8f6f4 v[88:91], v[170:177], v[196:203], v[88:91]
	v_mfma_f32_16x16x128_f8f6f4 v[76:79], v[162:169], v[204:211], v[76:79]
	v_mfma_f32_16x16x128_f8f6f4 v[72:75], v[170:177], v[204:211], v[72:75]
	s_setprio 0
	s_barrier
	ds_read_b128 v[218:221], v147 offset:49152
	ds_read_b128 v[226:229], v147 offset:51200
	ds_read_b128 v[222:225], v148 offset:49152
	ds_read_b128 v[230:233], v148 offset:51200
	s_barrier
	s_waitcnt lgkmcnt(0)
	s_setprio 1
	s_waitcnt lgkmcnt(0)
	v_mfma_f32_16x16x128_f8f6f4 v[116:119], v[218:225], v[178:185], v[116:119]
	v_mfma_f32_16x16x128_f8f6f4 v[112:115], v[226:233], v[178:185], v[112:115]
	v_mfma_f32_16x16x128_f8f6f4 v[100:103], v[218:225], v[186:193], v[100:103]
	v_mfma_f32_16x16x128_f8f6f4 v[96:99], v[226:233], v[186:193], v[96:99]
	v_mfma_f32_16x16x128_f8f6f4 v[84:87], v[218:225], v[196:203], v[84:87]
	v_mfma_f32_16x16x128_f8f6f4 v[80:83], v[226:233], v[196:203], v[80:83]
	v_mfma_f32_16x16x128_f8f6f4 v[68:71], v[218:225], v[204:211], v[68:71]
	v_mfma_f32_16x16x128_f8f6f4 v[64:67], v[226:233], v[204:211], v[64:67]
	s_setprio 0
	s_barrier
	s_mov_b32 m0, s69
	v_lshl_add_u64 v[212:213], v[212:213], 0, s[20:21]
	ds_read_b128 v[178:181], v145 offset:49152
	ds_read_b128 v[186:189], v145 offset:51200
	ds_read_b128 v[182:185], v146 offset:49152
	ds_read_b128 v[190:193], v146 offset:51200
	ds_read_b128 v[196:199], v145 offset:53248
	ds_read_b128 v[204:207], v145 offset:55296
	ds_read_b128 v[200:203], v146 offset:53248
	ds_read_b128 v[208:211], v146 offset:55296
	global_load_lds_dwordx4 v[212:213], off
	v_lshl_add_u64 v[212:213], v[214:215], 0, s[20:21]
	s_mov_b32 m0, s70
	s_nop 0
	global_load_lds_dwordx4 v[212:213], off
	s_waitcnt lgkmcnt(8)
	s_barrier
	s_waitcnt lgkmcnt(0)
	s_setprio 1
	s_waitcnt lgkmcnt(0)
	v_mfma_f32_16x16x128_f8f6f4 v[60:63], v[162:169], v[178:185], v[60:63]
	v_mfma_f32_16x16x128_f8f6f4 v[56:59], v[170:177], v[178:185], v[56:59]
	v_mfma_f32_16x16x128_f8f6f4 v[44:47], v[162:169], v[186:193], v[44:47]
	v_mfma_f32_16x16x128_f8f6f4 v[40:43], v[170:177], v[186:193], v[40:43]
	v_mfma_f32_16x16x128_f8f6f4 v[28:31], v[162:169], v[196:203], v[28:31]
	v_mfma_f32_16x16x128_f8f6f4 v[24:27], v[170:177], v[196:203], v[24:27]
	v_mfma_f32_16x16x128_f8f6f4 v[12:15], v[162:169], v[204:211], v[12:15]
	v_mfma_f32_16x16x128_f8f6f4 v[8:11], v[170:177], v[204:211], v[8:11]
	s_setprio 0
	s_barrier
	s_mov_b32 m0, s67
	v_lshl_add_u64 v[140:141], v[140:141], 0, s[20:21]
	global_load_lds_dwordx4 v[140:141], off
	v_lshl_add_u64 v[140:141], v[142:143], 0, s[20:21]
	s_mov_b32 m0, s68
	s_nop 0
	global_load_lds_dwordx4 v[140:141], off
	s_waitcnt vmcnt(4)
	s_waitcnt lgkmcnt(0)
	s_barrier
	s_setprio 1
	s_waitcnt lgkmcnt(0)
	v_mfma_f32_16x16x128_f8f6f4 v[52:55], v[218:225], v[178:185], v[52:55]
	v_mfma_f32_16x16x128_f8f6f4 v[48:51], v[226:233], v[178:185], v[48:51]
	v_mfma_f32_16x16x128_f8f6f4 v[36:39], v[218:225], v[186:193], v[36:39]
	v_mfma_f32_16x16x128_f8f6f4 v[32:35], v[226:233], v[186:193], v[32:35]
	v_mfma_f32_16x16x128_f8f6f4 v[20:23], v[218:225], v[196:203], v[20:23]
	v_mfma_f32_16x16x128_f8f6f4 v[16:19], v[226:233], v[196:203], v[16:19]
	v_mfma_f32_16x16x128_f8f6f4 v[4:7], v[218:225], v[204:211], v[4:7]
	v_mfma_f32_16x16x128_f8f6f4 v[0:3], v[226:233], v[204:211], v[0:3]
	s_setprio 0
	s_barrier
	s_mov_b32 m0, s71
	v_lshl_add_u64 v[140:141], s[44:45], 0, v[128:129]
	global_load_lds_dwordx4 v[140:141], off
	v_lshl_add_u64 v[140:141], s[44:45], 0, v[130:131]
	s_mov_b32 m0, s72
	s_andn2_b64 vcc, exec, s[40:41]
	global_load_lds_dwordx4 v[140:141], off
	s_mov_b64 s[42:43], -1
	s_mov_b64 s[40:41], 0
	s_mov_b64 s[44:45], 0x100
	s_cbranch_vccz .LBB0_1961
	s_branch .Lpeel_after_1961
.LBB0_1961:
	s_add_u32 s52, s12, s44
	s_addc_u32 s53, s13, s45
	s_add_u32 s29, s52, 0x100
	s_addc_u32 s48, s53, 0
	s_and_b64 s[46:47], s[42:43], exec
	s_cselect_b32 s46, s12, s29
	s_cselect_b32 s47, s13, s48
	s_add_u32 s29, s38, s44
	s_addc_u32 s44, s39, s45
	s_add_u32 s29, s29, 0x100
	s_addc_u32 s48, s44, 0
	ds_read_b128 v[162:165], v147
	ds_read_b128 v[170:173], v147 offset:2048
	ds_read_b128 v[166:169], v148
	ds_read_b128 v[174:177], v148 offset:2048
	s_and_b64 s[44:45], s[42:43], exec
	s_cselect_b32 s51, s35, s48
	s_cselect_b32 s50, s34, s29
	s_add_i32 m0, s0, 0xc000
	s_add_i32 s29, s0, 0xe000
	s_add_u32 s48, s50, 0x1000
	s_addc_u32 s49, s51, 0
	s_add_u32 s44, s50, 0x1080
	s_addc_u32 s45, s51, 0
	v_cndmask_b32_e64 v132, v135, v157, s[42:43]
	v_cndmask_b32_e64 v161, v136, v159, s[42:43]
	v_lshl_add_u64 v[140:141], s[52:53], 0, v[136:137]
	v_lshl_add_u64 v[140:141], v[140:141], 0, s[20:21]
	ds_read_b128 v[178:181], v145
	ds_read_b128 v[186:189], v145 offset:2048
	ds_read_b128 v[182:185], v146
	ds_read_b128 v[190:193], v146 offset:2048
	ds_read_b128 v[196:199], v145 offset:4096
	ds_read_b128 v[204:207], v145 offset:6144
	ds_read_b128 v[200:203], v146 offset:4096
	ds_read_b128 v[208:211], v146 offset:6144
	global_load_lds_dwordx4 v[140:141], off
	v_lshl_add_u64 v[140:141], s[52:53], 0, v[138:139]
	v_lshl_add_u64 v[140:141], v[140:141], 0, s[20:21]
	s_mov_b32 m0, s29
	s_nop 0
	global_load_lds_dwordx4 v[140:141], off
	s_waitcnt lgkmcnt(8)
	s_barrier
	s_waitcnt lgkmcnt(0)
	v_cndmask_b32_e64 v140, v134, v158, s[42:43]
	s_setprio 1
	s_waitcnt lgkmcnt(0)
	v_mfma_f32_16x16x128_f8f6f4 v[124:127], v[162:169], v[178:185], v[124:127]
	v_mfma_f32_16x16x128_f8f6f4 v[120:123], v[170:177], v[178:185], v[120:123]
	v_mfma_f32_16x16x128_f8f6f4 v[108:111], v[162:169], v[186:193], v[108:111]
	v_mfma_f32_16x16x128_f8f6f4 v[104:107], v[170:177], v[186:193], v[104:107]
	v_mfma_f32_16x16x128_f8f6f4 v[92:95], v[162:169], v[196:203], v[92:95]
	v_mfma_f32_16x16x128_f8f6f4 v[88:91], v[170:177], v[196:203], v[88:91]
	v_mfma_f32_16x16x128_f8f6f4 v[76:79], v[162:169], v[204:211], v[76:79]
	v_mfma_f32_16x16x128_f8f6f4 v[72:75], v[170:177], v[204:211], v[72:75]
	s_setprio 0
	s_barrier
	ds_read_b128 v[218:221], v147 offset:16384
	ds_read_b128 v[226:229], v147 offset:18432
	ds_read_b128 v[222:225], v148 offset:16384
	ds_read_b128 v[230:233], v148 offset:18432
	s_barrier
	s_waitcnt lgkmcnt(0)
	s_setprio 1
	s_waitcnt lgkmcnt(0)
	v_mfma_f32_16x16x128_f8f6f4 v[116:119], v[218:225], v[178:185], v[116:119]
	v_mfma_f32_16x16x128_f8f6f4 v[112:115], v[226:233], v[178:185], v[112:115]
	v_mfma_f32_16x16x128_f8f6f4 v[100:103], v[218:225], v[186:193], v[100:103]
	v_mfma_f32_16x16x128_f8f6f4 v[96:99], v[226:233], v[186:193], v[96:99]
	v_mfma_f32_16x16x128_f8f6f4 v[84:87], v[218:225], v[196:203], v[84:87]
	v_mfma_f32_16x16x128_f8f6f4 v[80:83], v[226:233], v[196:203], v[80:83]
	v_mfma_f32_16x16x128_f8f6f4 v[68:71], v[218:225], v[204:211], v[68:71]
	v_mfma_f32_16x16x128_f8f6f4 v[64:67], v[226:233], v[204:211], v[64:67]
	s_setprio 0
	s_barrier
	s_mov_b32 m0, s0
	ds_read_b128 v[178:181], v145 offset:16384
	ds_read_b128 v[186:189], v145 offset:18432
	ds_read_b128 v[182:185], v146 offset:16384
	ds_read_b128 v[190:193], v146 offset:18432
	ds_read_b128 v[196:199], v145 offset:20480
	ds_read_b128 v[204:207], v145 offset:22528
	ds_read_b128 v[200:203], v146 offset:20480
	ds_read_b128 v[208:211], v146 offset:22528
	global_load_lds_dwordx4 v132, s[46:47]
	s_mov_b32 m0, s56
	v_mov_b32_e32 v141, v133
	global_load_lds_dwordx4 v140, s[46:47]
	s_waitcnt lgkmcnt(8)
	s_barrier
	s_waitcnt lgkmcnt(0)
	v_lshl_add_u64 v[212:213], s[46:47], 0, v[132:133]
	v_lshl_add_u64 v[214:215], s[46:47], 0, v[140:141]
	s_setprio 1
	s_waitcnt lgkmcnt(0)
	v_mfma_f32_16x16x128_f8f6f4 v[60:63], v[162:169], v[178:185], v[60:63]
	v_mfma_f32_16x16x128_f8f6f4 v[56:59], v[170:177], v[178:185], v[56:59]
	v_mfma_f32_16x16x128_f8f6f4 v[44:47], v[162:169], v[186:193], v[44:47]
	v_mfma_f32_16x16x128_f8f6f4 v[40:43], v[170:177], v[186:193], v[40:43]
	v_mfma_f32_16x16x128_f8f6f4 v[28:31], v[162:169], v[196:203], v[28:31]
	v_mfma_f32_16x16x128_f8f6f4 v[24:27], v[170:177], v[196:203], v[24:27]
	v_mfma_f32_16x16x128_f8f6f4 v[12:15], v[162:169], v[204:211], v[12:15]
	v_mfma_f32_16x16x128_f8f6f4 v[8:11], v[170:177], v[204:211], v[8:11]
	s_setprio 0
	s_barrier
	s_mov_b32 m0, s1
	v_lshl_add_u64 v[140:141], s[50:51], 0, v[128:129]
	global_load_lds_dwordx4 v[140:141], off
	v_lshl_add_u64 v[142:143], s[50:51], 0, v[130:131]
	s_mov_b32 m0, s37
	s_nop 0
	global_load_lds_dwordx4 v[142:143], off
	s_waitcnt vmcnt(4)
	s_waitcnt lgkmcnt(0)
	s_barrier
	s_setprio 1
	s_waitcnt lgkmcnt(0)
	v_mfma_f32_16x16x128_f8f6f4 v[52:55], v[218:225], v[178:185], v[52:55]
	v_mfma_f32_16x16x128_f8f6f4 v[48:51], v[226:233], v[178:185], v[48:51]
	v_mfma_f32_16x16x128_f8f6f4 v[36:39], v[218:225], v[186:193], v[36:39]
	v_mfma_f32_16x16x128_f8f6f4 v[32:35], v[226:233], v[186:193], v[32:35]
	v_mfma_f32_16x16x128_f8f6f4 v[20:23], v[218:225], v[196:203], v[20:23]
	v_mfma_f32_16x16x128_f8f6f4 v[16:19], v[226:233], v[196:203], v[16:19]
	v_mfma_f32_16x16x128_f8f6f4 v[4:7], v[218:225], v[204:211], v[4:7]
	v_mfma_f32_16x16x128_f8f6f4 v[0:3], v[226:233], v[204:211], v[0:3]
	s_setprio 0
	s_barrier
	ds_read_b128 v[162:165], v147 offset:32768
	ds_read_b128 v[170:173], v147 offset:34816
	ds_read_b128 v[166:169], v148 offset:32768
	ds_read_b128 v[174:177], v148 offset:34816
	s_mov_b32 m0, s65
	ds_read_b128 v[178:181], v145 offset:32768
	ds_read_b128 v[186:189], v145 offset:34816
	ds_read_b128 v[182:185], v146 offset:32768
	ds_read_b128 v[190:193], v146 offset:34816
	ds_read_b128 v[196:199], v145 offset:36864
	ds_read_b128 v[204:207], v145 offset:38912
	ds_read_b128 v[200:203], v146 offset:36864
	ds_read_b128 v[208:211], v146 offset:38912
	v_cndmask_b32_e64 v132, v138, v160, s[42:43]
	global_load_lds_dwordx4 v161, s[46:47]
	s_mov_b32 m0, s66
	v_lshl_add_u64 v[216:217], s[48:49], 0, v[128:129]
	global_load_lds_dwordx4 v132, s[46:47]
	s_mov_b32 m0, s57
	s_nop 0
	global_load_lds_dwordx4 v[216:217], off
	v_lshl_add_u64 v[216:217], s[48:49], 0, v[130:131]
	s_mov_b32 m0, s64
	s_nop 0
	global_load_lds_dwordx4 v[216:217], off
	s_waitcnt lgkmcnt(8)
	s_barrier
	s_waitcnt lgkmcnt(0)
	s_setprio 1
	s_waitcnt lgkmcnt(0)
	v_mfma_f32_16x16x128_f8f6f4 v[124:127], v[162:169], v[178:185], v[124:127]
	v_mfma_f32_16x16x128_f8f6f4 v[120:123], v[170:177], v[178:185], v[120:123]
	v_mfma_f32_16x16x128_f8f6f4 v[108:111], v[162:169], v[186:193], v[108:111]
	v_mfma_f32_16x16x128_f8f6f4 v[104:107], v[170:177], v[186:193], v[104:107]
	v_mfma_f32_16x16x128_f8f6f4 v[92:95], v[162:169], v[196:203], v[92:95]
	v_mfma_f32_16x16x128_f8f6f4 v[88:91], v[170:177], v[196:203], v[88:91]
	v_mfma_f32_16x16x128_f8f6f4 v[76:79], v[162:169], v[204:211], v[76:79]
	v_mfma_f32_16x16x128_f8f6f4 v[72:75], v[170:177], v[204:211], v[72:75]
	s_setprio 0
	s_barrier
	ds_read_b128 v[218:221], v147 offset:49152
	ds_read_b128 v[226:229], v147 offset:51200
	ds_read_b128 v[222:225], v148 offset:49152
	ds_read_b128 v[230:233], v148 offset:51200
	s_barrier
	s_waitcnt lgkmcnt(0)
	s_setprio 1
	s_waitcnt lgkmcnt(0)
	v_mfma_f32_16x16x128_f8f6f4 v[116:119], v[218:225], v[178:185], v[116:119]
	v_mfma_f32_16x16x128_f8f6f4 v[112:115], v[226:233], v[178:185], v[112:115]
	v_mfma_f32_16x16x128_f8f6f4 v[100:103], v[218:225], v[186:193], v[100:103]
	v_mfma_f32_16x16x128_f8f6f4 v[96:99], v[226:233], v[186:193], v[96:99]
	v_mfma_f32_16x16x128_f8f6f4 v[84:87], v[218:225], v[196:203], v[84:87]
	v_mfma_f32_16x16x128_f8f6f4 v[80:83], v[226:233], v[196:203], v[80:83]
	v_mfma_f32_16x16x128_f8f6f4 v[68:71], v[218:225], v[204:211], v[68:71]
	v_mfma_f32_16x16x128_f8f6f4 v[64:67], v[226:233], v[204:211], v[64:67]
	s_setprio 0
	s_barrier
	s_mov_b32 m0, s69
	v_lshl_add_u64 v[212:213], v[212:213], 0, s[20:21]
	ds_read_b128 v[178:181], v145 offset:49152
	ds_read_b128 v[186:189], v145 offset:51200
	ds_read_b128 v[182:185], v146 offset:49152
	ds_read_b128 v[190:193], v146 offset:51200
	ds_read_b128 v[196:199], v145 offset:53248
	ds_read_b128 v[204:207], v145 offset:55296
	ds_read_b128 v[200:203], v146 offset:53248
	ds_read_b128 v[208:211], v146 offset:55296
	global_load_lds_dwordx4 v[212:213], off
	v_lshl_add_u64 v[212:213], v[214:215], 0, s[20:21]
	s_mov_b32 m0, s70
	s_nop 0
	global_load_lds_dwordx4 v[212:213], off
	s_waitcnt lgkmcnt(8)
	s_barrier
	s_waitcnt lgkmcnt(0)
	s_setprio 1
	s_waitcnt lgkmcnt(0)
	v_mfma_f32_16x16x128_f8f6f4 v[60:63], v[162:169], v[178:185], v[60:63]
	v_mfma_f32_16x16x128_f8f6f4 v[56:59], v[170:177], v[178:185], v[56:59]
	v_mfma_f32_16x16x128_f8f6f4 v[44:47], v[162:169], v[186:193], v[44:47]
	v_mfma_f32_16x16x128_f8f6f4 v[40:43], v[170:177], v[186:193], v[40:43]
	v_mfma_f32_16x16x128_f8f6f4 v[28:31], v[162:169], v[196:203], v[28:31]
	v_mfma_f32_16x16x128_f8f6f4 v[24:27], v[170:177], v[196:203], v[24:27]
	v_mfma_f32_16x16x128_f8f6f4 v[12:15], v[162:169], v[204:211], v[12:15]
	v_mfma_f32_16x16x128_f8f6f4 v[8:11], v[170:177], v[204:211], v[8:11]
	s_setprio 0
	s_barrier
	s_mov_b32 m0, s67
	v_lshl_add_u64 v[140:141], v[140:141], 0, s[20:21]
	global_load_lds_dwordx4 v[140:141], off
	v_lshl_add_u64 v[140:141], v[142:143], 0, s[20:21]
	s_mov_b32 m0, s68
	s_nop 0
	global_load_lds_dwordx4 v[140:141], off
	s_waitcnt vmcnt(4)
	s_waitcnt lgkmcnt(0)
	s_barrier
	s_setprio 1
	s_waitcnt lgkmcnt(0)
	v_mfma_f32_16x16x128_f8f6f4 v[52:55], v[218:225], v[178:185], v[52:55]
	v_mfma_f32_16x16x128_f8f6f4 v[48:51], v[226:233], v[178:185], v[48:51]
	v_mfma_f32_16x16x128_f8f6f4 v[36:39], v[218:225], v[186:193], v[36:39]
	v_mfma_f32_16x16x128_f8f6f4 v[32:35], v[226:233], v[186:193], v[32:35]
	v_mfma_f32_16x16x128_f8f6f4 v[20:23], v[218:225], v[196:203], v[20:23]
	v_mfma_f32_16x16x128_f8f6f4 v[16:19], v[226:233], v[196:203], v[16:19]
	v_mfma_f32_16x16x128_f8f6f4 v[4:7], v[218:225], v[204:211], v[4:7]
	v_mfma_f32_16x16x128_f8f6f4 v[0:3], v[226:233], v[204:211], v[0:3]
	s_setprio 0
	s_barrier
	s_mov_b32 m0, s71
	v_lshl_add_u64 v[140:141], s[44:45], 0, v[128:129]
	global_load_lds_dwordx4 v[140:141], off
	v_lshl_add_u64 v[140:141], s[44:45], 0, v[130:131]
	s_mov_b32 m0, s72
	s_andn2_b64 vcc, exec, s[40:41]
	global_load_lds_dwordx4 v[140:141], off
	s_mov_b64 s[42:43], -1
	s_mov_b64 s[40:41], 0
	s_mov_b64 s[44:45], 0x100
	s_cbranch_vccz .LBB0_1961

.LBB0_1988:
	v_mov_b32_e32 v137, v133
	v_mov_b32_e32 v139, v133
	s_mov_b64 s[34:35], 0
	s_mov_b64 s[28:29], -1
	s_mov_b64 s[30:31], 0
	s_add_u32 s42, s10, s34
	s_addc_u32 s43, s11, s35
	s_add_u32 s38, s42, 0x100
	s_addc_u32 s39, s43, 0
	s_and_b64 s[36:37], s[30:31], exec
	s_cselect_b32 s36, s10, s38
	s_cselect_b32 s37, s11, s39
	s_add_u32 s34, s26, s34
	s_addc_u32 s35, s27, s35
	s_add_u32 s38, s34, 0x100
	s_addc_u32 s39, s35, 0
	ds_read_b128 v[160:163], v147
	ds_read_b128 v[168:171], v147 offset:2048
	ds_read_b128 v[164:167], v148
	ds_read_b128 v[172:175], v148 offset:2048
	s_and_b64 s[34:35], s[30:31], exec
	s_cselect_b32 s41, s25, s39
	s_cselect_b32 s40, s24, s38
	s_add_i32 m0, s0, 0xc000
	s_add_i32 s62, s0, 0xe000
	s_add_u32 s38, s40, 0x1000
	s_addc_u32 s39, s41, 0
	s_add_u32 s34, s40, 0x1080
	s_addc_u32 s35, s41, 0
	v_cndmask_b32_e64 v132, v135, v155, s[30:31]
	v_cndmask_b32_e64 v159, v136, v157, s[30:31]
	v_lshl_add_u64 v[140:141], s[42:43], 0, v[136:137]
	v_lshl_add_u64 v[140:141], v[140:141], 0, s[16:17]
	ds_read_b128 v[176:179], v145
	ds_read_b128 v[184:187], v145 offset:2048
	ds_read_b128 v[180:183], v146
	ds_read_b128 v[188:191], v146 offset:2048
	ds_read_b128 v[196:199], v145 offset:4096
	ds_read_b128 v[204:207], v145 offset:6144
	ds_read_b128 v[200:203], v146 offset:4096
	ds_read_b128 v[208:211], v146 offset:6144
	global_load_lds_dwordx4 v[140:141], off
	v_lshl_add_u64 v[140:141], s[42:43], 0, v[138:139]
	v_lshl_add_u64 v[140:141], v[140:141], 0, s[16:17]
	s_mov_b32 m0, s62
	s_nop 0
	global_load_lds_dwordx4 v[140:141], off
	s_waitcnt lgkmcnt(8)
	s_barrier
	s_waitcnt lgkmcnt(0)
	v_cndmask_b32_e64 v140, v134, v156, s[30:31]
	s_setprio 1
	s_waitcnt lgkmcnt(0)
	v_mfma_f32_16x16x128_f8f6f4 v[124:127], v[160:167], v[176:183], 0
	v_mfma_f32_16x16x128_f8f6f4 v[120:123], v[168:175], v[176:183], 0
	v_mfma_f32_16x16x128_f8f6f4 v[108:111], v[160:167], v[184:191], 0
	v_mfma_f32_16x16x128_f8f6f4 v[104:107], v[168:175], v[184:191], 0
	v_mfma_f32_16x16x128_f8f6f4 v[92:95], v[160:167], v[196:203], 0
	v_mfma_f32_16x16x128_f8f6f4 v[88:91], v[168:175], v[196:203], 0
	v_mfma_f32_16x16x128_f8f6f4 v[76:79], v[160:167], v[204:211], 0
	v_mfma_f32_16x16x128_f8f6f4 v[72:75], v[168:175], v[204:211], 0
	s_setprio 0
	s_barrier
	ds_read_b128 v[218:221], v147 offset:16384
	ds_read_b128 v[226:229], v147 offset:18432
	ds_read_b128 v[222:225], v148 offset:16384
	ds_read_b128 v[230:233], v148 offset:18432
	s_barrier
	s_waitcnt lgkmcnt(0)
	s_setprio 1
	s_waitcnt lgkmcnt(0)
	v_mfma_f32_16x16x128_f8f6f4 v[116:119], v[218:225], v[176:183], 0
	v_mfma_f32_16x16x128_f8f6f4 v[112:115], v[226:233], v[176:183], 0
	v_mfma_f32_16x16x128_f8f6f4 v[100:103], v[218:225], v[184:191], 0
	v_mfma_f32_16x16x128_f8f6f4 v[96:99], v[226:233], v[184:191], 0
	v_mfma_f32_16x16x128_f8f6f4 v[84:87], v[218:225], v[196:203], 0
	v_mfma_f32_16x16x128_f8f6f4 v[80:83], v[226:233], v[196:203], 0
	v_mfma_f32_16x16x128_f8f6f4 v[68:71], v[218:225], v[204:211], 0
	v_mfma_f32_16x16x128_f8f6f4 v[64:67], v[226:233], v[204:211], 0
	s_setprio 0
	s_barrier
	s_mov_b32 m0, s0
	ds_read_b128 v[176:179], v145 offset:16384
	ds_read_b128 v[184:187], v145 offset:18432
	ds_read_b128 v[180:183], v146 offset:16384
	ds_read_b128 v[188:191], v146 offset:18432
	ds_read_b128 v[196:199], v145 offset:20480
	ds_read_b128 v[204:207], v145 offset:22528
	ds_read_b128 v[200:203], v146 offset:20480
	ds_read_b128 v[208:211], v146 offset:22528
	global_load_lds_dwordx4 v132, s[36:37]
	s_mov_b32 m0, s47
	v_mov_b32_e32 v141, v133
	global_load_lds_dwordx4 v140, s[36:37]
	s_waitcnt lgkmcnt(8)
	s_barrier
	s_waitcnt lgkmcnt(0)
	v_lshl_add_u64 v[192:193], s[36:37], 0, v[132:133]
	v_lshl_add_u64 v[212:213], s[36:37], 0, v[140:141]
	s_setprio 1
	s_waitcnt lgkmcnt(0)
	v_mfma_f32_16x16x128_f8f6f4 v[60:63], v[160:167], v[176:183], 0
	v_mfma_f32_16x16x128_f8f6f4 v[56:59], v[168:175], v[176:183], 0
	v_mfma_f32_16x16x128_f8f6f4 v[44:47], v[160:167], v[184:191], 0
	v_mfma_f32_16x16x128_f8f6f4 v[40:43], v[168:175], v[184:191], 0
	v_mfma_f32_16x16x128_f8f6f4 v[28:31], v[160:167], v[196:203], 0
	v_mfma_f32_16x16x128_f8f6f4 v[24:27], v[168:175], v[196:203], 0
	v_mfma_f32_16x16x128_f8f6f4 v[12:15], v[160:167], v[204:211], 0
	v_mfma_f32_16x16x128_f8f6f4 v[8:11], v[168:175], v[204:211], 0
	s_setprio 0
	s_barrier
	s_mov_b32 m0, s1
	v_lshl_add_u64 v[140:141], s[40:41], 0, v[128:129]
	global_load_lds_dwordx4 v[140:141], off
	v_lshl_add_u64 v[142:143], s[40:41], 0, v[130:131]
	s_mov_b32 m0, s46
	s_nop 0
	global_load_lds_dwordx4 v[142:143], off
	s_waitcnt vmcnt(4)
	s_waitcnt lgkmcnt(0)
	s_barrier
	s_setprio 1
	s_waitcnt lgkmcnt(0)
	v_mfma_f32_16x16x128_f8f6f4 v[52:55], v[218:225], v[176:183], 0
	v_mfma_f32_16x16x128_f8f6f4 v[48:51], v[226:233], v[176:183], 0
	v_mfma_f32_16x16x128_f8f6f4 v[36:39], v[218:225], v[184:191], 0
	v_mfma_f32_16x16x128_f8f6f4 v[32:35], v[226:233], v[184:191], 0
	v_mfma_f32_16x16x128_f8f6f4 v[20:23], v[218:225], v[196:203], 0
	v_mfma_f32_16x16x128_f8f6f4 v[16:19], v[226:233], v[196:203], 0
	v_mfma_f32_16x16x128_f8f6f4 v[4:7], v[218:225], v[204:211], 0
	v_mfma_f32_16x16x128_f8f6f4 v[0:3], v[226:233], v[204:211], 0
	s_setprio 0
	s_barrier
	ds_read_b128 v[160:163], v147 offset:32768
	ds_read_b128 v[168:171], v147 offset:34816
	ds_read_b128 v[164:167], v148 offset:32768
	ds_read_b128 v[172:175], v148 offset:34816
	s_mov_b32 m0, s50
	ds_read_b128 v[176:179], v145 offset:32768
	ds_read_b128 v[184:187], v145 offset:34816
	ds_read_b128 v[180:183], v146 offset:32768
	ds_read_b128 v[188:191], v146 offset:34816
	ds_read_b128 v[196:199], v145 offset:36864
	ds_read_b128 v[204:207], v145 offset:38912
	ds_read_b128 v[200:203], v146 offset:36864
	ds_read_b128 v[208:211], v146 offset:38912
	v_cndmask_b32_e64 v132, v138, v158, s[30:31]
	global_load_lds_dwordx4 v159, s[36:37]
	s_mov_b32 m0, s51
	v_lshl_add_u64 v[214:215], s[38:39], 0, v[128:129]
	global_load_lds_dwordx4 v132, s[36:37]
	s_mov_b32 m0, s48
	s_nop 0
	global_load_lds_dwordx4 v[214:215], off
	v_lshl_add_u64 v[214:215], s[38:39], 0, v[130:131]
	s_mov_b32 m0, s49
	s_nop 0
	global_load_lds_dwordx4 v[214:215], off
	s_waitcnt lgkmcnt(8)
	s_barrier
	s_waitcnt lgkmcnt(0)
	s_setprio 1
	s_waitcnt lgkmcnt(0)
	v_mfma_f32_16x16x128_f8f6f4 v[124:127], v[160:167], v[176:183], v[124:127]
	v_mfma_f32_16x16x128_f8f6f4 v[120:123], v[168:175], v[176:183], v[120:123]
	v_mfma_f32_16x16x128_f8f6f4 v[108:111], v[160:167], v[184:191], v[108:111]
	v_mfma_f32_16x16x128_f8f6f4 v[104:107], v[168:175], v[184:191], v[104:107]
	v_mfma_f32_16x16x128_f8f6f4 v[92:95], v[160:167], v[196:203], v[92:95]
	v_mfma_f32_16x16x128_f8f6f4 v[88:91], v[168:175], v[196:203], v[88:91]
	v_mfma_f32_16x16x128_f8f6f4 v[76:79], v[160:167], v[204:211], v[76:79]
	v_mfma_f32_16x16x128_f8f6f4 v[72:75], v[168:175], v[204:211], v[72:75]
	s_setprio 0
	s_barrier
	ds_read_b128 v[218:221], v147 offset:49152
	ds_read_b128 v[226:229], v147 offset:51200
	ds_read_b128 v[222:225], v148 offset:49152
	ds_read_b128 v[230:233], v148 offset:51200
	s_barrier
	s_waitcnt lgkmcnt(0)
	s_setprio 1
	s_waitcnt lgkmcnt(0)
	v_mfma_f32_16x16x128_f8f6f4 v[116:119], v[218:225], v[176:183], v[116:119]
	v_mfma_f32_16x16x128_f8f6f4 v[112:115], v[226:233], v[176:183], v[112:115]
	v_mfma_f32_16x16x128_f8f6f4 v[100:103], v[218:225], v[184:191], v[100:103]
	v_mfma_f32_16x16x128_f8f6f4 v[96:99], v[226:233], v[184:191], v[96:99]
	v_mfma_f32_16x16x128_f8f6f4 v[84:87], v[218:225], v[196:203], v[84:87]
	v_mfma_f32_16x16x128_f8f6f4 v[80:83], v[226:233], v[196:203], v[80:83]
	v_mfma_f32_16x16x128_f8f6f4 v[68:71], v[218:225], v[204:211], v[68:71]
	v_mfma_f32_16x16x128_f8f6f4 v[64:67], v[226:233], v[204:211], v[64:67]
	s_setprio 0
	s_barrier
	s_mov_b32 m0, s55
	v_lshl_add_u64 v[192:193], v[192:193], 0, s[16:17]
	ds_read_b128 v[176:179], v145 offset:49152
	ds_read_b128 v[184:187], v145 offset:51200
	ds_read_b128 v[180:183], v146 offset:49152
	ds_read_b128 v[188:191], v146 offset:51200
	ds_read_b128 v[196:199], v145 offset:53248
	ds_read_b128 v[204:207], v145 offset:55296
	ds_read_b128 v[200:203], v146 offset:53248
	ds_read_b128 v[208:211], v146 offset:55296
	global_load_lds_dwordx4 v[192:193], off
	v_lshl_add_u64 v[192:193], v[212:213], 0, s[16:17]
	s_mov_b32 m0, s56
	s_nop 0
	global_load_lds_dwordx4 v[192:193], off
	s_waitcnt lgkmcnt(8)
	s_barrier
	s_waitcnt lgkmcnt(0)
	s_setprio 1
	s_waitcnt lgkmcnt(0)
	v_mfma_f32_16x16x128_f8f6f4 v[60:63], v[160:167], v[176:183], v[60:63]
	v_mfma_f32_16x16x128_f8f6f4 v[56:59], v[168:175], v[176:183], v[56:59]
	v_mfma_f32_16x16x128_f8f6f4 v[44:47], v[160:167], v[184:191], v[44:47]
	v_mfma_f32_16x16x128_f8f6f4 v[40:43], v[168:175], v[184:191], v[40:43]
	v_mfma_f32_16x16x128_f8f6f4 v[28:31], v[160:167], v[196:203], v[28:31]
	v_mfma_f32_16x16x128_f8f6f4 v[24:27], v[168:175], v[196:203], v[24:27]
	v_mfma_f32_16x16x128_f8f6f4 v[12:15], v[160:167], v[204:211], v[12:15]
	v_mfma_f32_16x16x128_f8f6f4 v[8:11], v[168:175], v[204:211], v[8:11]
	s_setprio 0
	s_barrier
	s_mov_b32 m0, s53
	v_lshl_add_u64 v[140:141], v[140:141], 0, s[16:17]
	global_load_lds_dwordx4 v[140:141], off
	v_lshl_add_u64 v[140:141], v[142:143], 0, s[16:17]
	s_mov_b32 m0, s54
	s_nop 0
	global_load_lds_dwordx4 v[140:141], off
	s_waitcnt vmcnt(4)
	s_waitcnt lgkmcnt(0)
	s_barrier
	s_setprio 1
	s_waitcnt lgkmcnt(0)
	v_mfma_f32_16x16x128_f8f6f4 v[52:55], v[218:225], v[176:183], v[52:55]
	v_mfma_f32_16x16x128_f8f6f4 v[48:51], v[226:233], v[176:183], v[48:51]
	v_mfma_f32_16x16x128_f8f6f4 v[36:39], v[218:225], v[184:191], v[36:39]
	v_mfma_f32_16x16x128_f8f6f4 v[32:35], v[226:233], v[184:191], v[32:35]
	v_mfma_f32_16x16x128_f8f6f4 v[20:23], v[218:225], v[196:203], v[20:23]
	v_mfma_f32_16x16x128_f8f6f4 v[16:19], v[226:233], v[196:203], v[16:19]
	v_mfma_f32_16x16x128_f8f6f4 v[4:7], v[218:225], v[204:211], v[4:7]
	v_mfma_f32_16x16x128_f8f6f4 v[0:3], v[226:233], v[204:211], v[0:3]
	s_setprio 0
	s_barrier
	s_mov_b32 m0, s57
	v_lshl_add_u64 v[140:141], s[34:35], 0, v[128:129]
	global_load_lds_dwordx4 v[140:141], off
	v_lshl_add_u64 v[140:141], s[34:35], 0, v[130:131]
	s_mov_b32 m0, s58
	s_andn2_b64 vcc, exec, s[28:29]
	global_load_lds_dwordx4 v[140:141], off
	s_mov_b64 s[30:31], -1
	s_mov_b64 s[28:29], 0
	s_mov_b64 s[34:35], 0x100
	s_cbranch_vccz .LBB0_1989
	s_branch .Lpeel_after_1989
.LBB0_1989:
	s_add_u32 s42, s10, s34
	s_addc_u32 s43, s11, s35
	s_add_u32 s38, s42, 0x100
	s_addc_u32 s39, s43, 0
	s_and_b64 s[36:37], s[30:31], exec
	s_cselect_b32 s36, s10, s38
	s_cselect_b32 s37, s11, s39
	s_add_u32 s34, s26, s34
	s_addc_u32 s35, s27, s35
	s_add_u32 s38, s34, 0x100
	s_addc_u32 s39, s35, 0
	ds_read_b128 v[160:163], v147
	ds_read_b128 v[168:171], v147 offset:2048
	ds_read_b128 v[164:167], v148
	ds_read_b128 v[172:175], v148 offset:2048
	s_and_b64 s[34:35], s[30:31], exec
	s_cselect_b32 s41, s25, s39
	s_cselect_b32 s40, s24, s38
	s_add_i32 m0, s0, 0xc000
	s_add_i32 s62, s0, 0xe000
	s_add_u32 s38, s40, 0x1000
	s_addc_u32 s39, s41, 0
	s_add_u32 s34, s40, 0x1080
	s_addc_u32 s35, s41, 0
	v_cndmask_b32_e64 v132, v135, v155, s[30:31]
	v_cndmask_b32_e64 v159, v136, v157, s[30:31]
	v_lshl_add_u64 v[140:141], s[42:43], 0, v[136:137]
	v_lshl_add_u64 v[140:141], v[140:141], 0, s[16:17]
	ds_read_b128 v[176:179], v145
	ds_read_b128 v[184:187], v145 offset:2048
	ds_read_b128 v[180:183], v146
	ds_read_b128 v[188:191], v146 offset:2048
	ds_read_b128 v[196:199], v145 offset:4096
	ds_read_b128 v[204:207], v145 offset:6144
	ds_read_b128 v[200:203], v146 offset:4096
	ds_read_b128 v[208:211], v146 offset:6144
	global_load_lds_dwordx4 v[140:141], off
	v_lshl_add_u64 v[140:141], s[42:43], 0, v[138:139]
	v_lshl_add_u64 v[140:141], v[140:141], 0, s[16:17]
	s_mov_b32 m0, s62
	s_nop 0
	global_load_lds_dwordx4 v[140:141], off
	s_waitcnt lgkmcnt(8)
	s_barrier
	s_waitcnt lgkmcnt(0)
	v_cndmask_b32_e64 v140, v134, v156, s[30:31]
	s_setprio 1
	s_waitcnt lgkmcnt(0)
	v_mfma_f32_16x16x128_f8f6f4 v[124:127], v[160:167], v[176:183], v[124:127]
	v_mfma_f32_16x16x128_f8f6f4 v[120:123], v[168:175], v[176:183], v[120:123]
	v_mfma_f32_16x16x128_f8f6f4 v[108:111], v[160:167], v[184:191], v[108:111]
	v_mfma_f32_16x16x128_f8f6f4 v[104:107], v[168:175], v[184:191], v[104:107]
	v_mfma_f32_16x16x128_f8f6f4 v[92:95], v[160:167], v[196:203], v[92:95]
	v_mfma_f32_16x16x128_f8f6f4 v[88:91], v[168:175], v[196:203], v[88:91]
	v_mfma_f32_16x16x128_f8f6f4 v[76:79], v[160:167], v[204:211], v[76:79]
	v_mfma_f32_16x16x128_f8f6f4 v[72:75], v[168:175], v[204:211], v[72:75]
	s_setprio 0
	s_barrier
	ds_read_b128 v[218:221], v147 offset:16384
	ds_read_b128 v[226:229], v147 offset:18432
	ds_read_b128 v[222:225], v148 offset:16384
	ds_read_b128 v[230:233], v148 offset:18432
	s_barrier
	s_waitcnt lgkmcnt(0)
	s_setprio 1
	s_waitcnt lgkmcnt(0)
	v_mfma_f32_16x16x128_f8f6f4 v[116:119], v[218:225], v[176:183], v[116:119]
	v_mfma_f32_16x16x128_f8f6f4 v[112:115], v[226:233], v[176:183], v[112:115]
	v_mfma_f32_16x16x128_f8f6f4 v[100:103], v[218:225], v[184:191], v[100:103]
	v_mfma_f32_16x16x128_f8f6f4 v[96:99], v[226:233], v[184:191], v[96:99]
	v_mfma_f32_16x16x128_f8f6f4 v[84:87], v[218:225], v[196:203], v[84:87]
	v_mfma_f32_16x16x128_f8f6f4 v[80:83], v[226:233], v[196:203], v[80:83]
	v_mfma_f32_16x16x128_f8f6f4 v[68:71], v[218:225], v[204:211], v[68:71]
	v_mfma_f32_16x16x128_f8f6f4 v[64:67], v[226:233], v[204:211], v[64:67]
	s_setprio 0
	s_barrier
	s_mov_b32 m0, s0
	ds_read_b128 v[176:179], v145 offset:16384
	ds_read_b128 v[184:187], v145 offset:18432
	ds_read_b128 v[180:183], v146 offset:16384
	ds_read_b128 v[188:191], v146 offset:18432
	ds_read_b128 v[196:199], v145 offset:20480
	ds_read_b128 v[204:207], v145 offset:22528
	ds_read_b128 v[200:203], v146 offset:20480
	ds_read_b128 v[208:211], v146 offset:22528
	global_load_lds_dwordx4 v132, s[36:37]
	s_mov_b32 m0, s47
	v_mov_b32_e32 v141, v133
	global_load_lds_dwordx4 v140, s[36:37]
	s_waitcnt lgkmcnt(8)
	s_barrier
	s_waitcnt lgkmcnt(0)
	v_lshl_add_u64 v[192:193], s[36:37], 0, v[132:133]
	v_lshl_add_u64 v[212:213], s[36:37], 0, v[140:141]
	s_setprio 1
	s_waitcnt lgkmcnt(0)
	v_mfma_f32_16x16x128_f8f6f4 v[60:63], v[160:167], v[176:183], v[60:63]
	v_mfma_f32_16x16x128_f8f6f4 v[56:59], v[168:175], v[176:183], v[56:59]
	v_mfma_f32_16x16x128_f8f6f4 v[44:47], v[160:167], v[184:191], v[44:47]
	v_mfma_f32_16x16x128_f8f6f4 v[40:43], v[168:175], v[184:191], v[40:43]
	v_mfma_f32_16x16x128_f8f6f4 v[28:31], v[160:167], v[196:203], v[28:31]
	v_mfma_f32_16x16x128_f8f6f4 v[24:27], v[168:175], v[196:203], v[24:27]
	v_mfma_f32_16x16x128_f8f6f4 v[12:15], v[160:167], v[204:211], v[12:15]
	v_mfma_f32_16x16x128_f8f6f4 v[8:11], v[168:175], v[204:211], v[8:11]
	s_setprio 0
	s_barrier
	s_mov_b32 m0, s1
	v_lshl_add_u64 v[140:141], s[40:41], 0, v[128:129]
	global_load_lds_dwordx4 v[140:141], off
	v_lshl_add_u64 v[142:143], s[40:41], 0, v[130:131]
	s_mov_b32 m0, s46
	s_nop 0
	global_load_lds_dwordx4 v[142:143], off
	s_waitcnt vmcnt(4)
	s_waitcnt lgkmcnt(0)
	s_barrier
	s_setprio 1
	s_waitcnt lgkmcnt(0)
	v_mfma_f32_16x16x128_f8f6f4 v[52:55], v[218:225], v[176:183], v[52:55]
	v_mfma_f32_16x16x128_f8f6f4 v[48:51], v[226:233], v[176:183], v[48:51]
	v_mfma_f32_16x16x128_f8f6f4 v[36:39], v[218:225], v[184:191], v[36:39]
	v_mfma_f32_16x16x128_f8f6f4 v[32:35], v[226:233], v[184:191], v[32:35]
	v_mfma_f32_16x16x128_f8f6f4 v[20:23], v[218:225], v[196:203], v[20:23]
	v_mfma_f32_16x16x128_f8f6f4 v[16:19], v[226:233], v[196:203], v[16:19]
	v_mfma_f32_16x16x128_f8f6f4 v[4:7], v[218:225], v[204:211], v[4:7]
	v_mfma_f32_16x16x128_f8f6f4 v[0:3], v[226:233], v[204:211], v[0:3]
	s_setprio 0
	s_barrier
	ds_read_b128 v[160:163], v147 offset:32768
	ds_read_b128 v[168:171], v147 offset:34816
	ds_read_b128 v[164:167], v148 offset:32768
	ds_read_b128 v[172:175], v148 offset:34816
	s_mov_b32 m0, s50
	ds_read_b128 v[176:179], v145 offset:32768
	ds_read_b128 v[184:187], v145 offset:34816
	ds_read_b128 v[180:183], v146 offset:32768
	ds_read_b128 v[188:191], v146 offset:34816
	ds_read_b128 v[196:199], v145 offset:36864
	ds_read_b128 v[204:207], v145 offset:38912
	ds_read_b128 v[200:203], v146 offset:36864
	ds_read_b128 v[208:211], v146 offset:38912
	v_cndmask_b32_e64 v132, v138, v158, s[30:31]
	global_load_lds_dwordx4 v159, s[36:37]
	s_mov_b32 m0, s51
	v_lshl_add_u64 v[214:215], s[38:39], 0, v[128:129]
	global_load_lds_dwordx4 v132, s[36:37]
	s_mov_b32 m0, s48
	s_nop 0
	global_load_lds_dwordx4 v[214:215], off
	v_lshl_add_u64 v[214:215], s[38:39], 0, v[130:131]
	s_mov_b32 m0, s49
	s_nop 0
	global_load_lds_dwordx4 v[214:215], off
	s_waitcnt lgkmcnt(8)
	s_barrier
	s_waitcnt lgkmcnt(0)
	s_setprio 1
	s_waitcnt lgkmcnt(0)
	v_mfma_f32_16x16x128_f8f6f4 v[124:127], v[160:167], v[176:183], v[124:127]
	v_mfma_f32_16x16x128_f8f6f4 v[120:123], v[168:175], v[176:183], v[120:123]
	v_mfma_f32_16x16x128_f8f6f4 v[108:111], v[160:167], v[184:191], v[108:111]
	v_mfma_f32_16x16x128_f8f6f4 v[104:107], v[168:175], v[184:191], v[104:107]
	v_mfma_f32_16x16x128_f8f6f4 v[92:95], v[160:167], v[196:203], v[92:95]
	v_mfma_f32_16x16x128_f8f6f4 v[88:91], v[168:175], v[196:203], v[88:91]
	v_mfma_f32_16x16x128_f8f6f4 v[76:79], v[160:167], v[204:211], v[76:79]
	v_mfma_f32_16x16x128_f8f6f4 v[72:75], v[168:175], v[204:211], v[72:75]
	s_setprio 0
	s_barrier
	ds_read_b128 v[218:221], v147 offset:49152
	ds_read_b128 v[226:229], v147 offset:51200
	ds_read_b128 v[222:225], v148 offset:49152
	ds_read_b128 v[230:233], v148 offset:51200
	s_barrier
	s_waitcnt lgkmcnt(0)
	s_setprio 1
	s_waitcnt lgkmcnt(0)
	v_mfma_f32_16x16x128_f8f6f4 v[116:119], v[218:225], v[176:183], v[116:119]
	v_mfma_f32_16x16x128_f8f6f4 v[112:115], v[226:233], v[176:183], v[112:115]
	v_mfma_f32_16x16x128_f8f6f4 v[100:103], v[218:225], v[184:191], v[100:103]
	v_mfma_f32_16x16x128_f8f6f4 v[96:99], v[226:233], v[184:191], v[96:99]
	v_mfma_f32_16x16x128_f8f6f4 v[84:87], v[218:225], v[196:203], v[84:87]
	v_mfma_f32_16x16x128_f8f6f4 v[80:83], v[226:233], v[196:203], v[80:83]
	v_mfma_f32_16x16x128_f8f6f4 v[68:71], v[218:225], v[204:211], v[68:71]
	v_mfma_f32_16x16x128_f8f6f4 v[64:67], v[226:233], v[204:211], v[64:67]
	s_setprio 0
	s_barrier
	s_mov_b32 m0, s55
	v_lshl_add_u64 v[192:193], v[192:193], 0, s[16:17]
	ds_read_b128 v[176:179], v145 offset:49152
	ds_read_b128 v[184:187], v145 offset:51200
	ds_read_b128 v[180:183], v146 offset:49152
	ds_read_b128 v[188:191], v146 offset:51200
	ds_read_b128 v[196:199], v145 offset:53248
	ds_read_b128 v[204:207], v145 offset:55296
	ds_read_b128 v[200:203], v146 offset:53248
	ds_read_b128 v[208:211], v146 offset:55296
	global_load_lds_dwordx4 v[192:193], off
	v_lshl_add_u64 v[192:193], v[212:213], 0, s[16:17]
	s_mov_b32 m0, s56
	s_nop 0
	global_load_lds_dwordx4 v[192:193], off
	s_waitcnt lgkmcnt(8)
	s_barrier
	s_waitcnt lgkmcnt(0)
	s_setprio 1
	s_waitcnt lgkmcnt(0)
	v_mfma_f32_16x16x128_f8f6f4 v[60:63], v[160:167], v[176:183], v[60:63]
	v_mfma_f32_16x16x128_f8f6f4 v[56:59], v[168:175], v[176:183], v[56:59]
	v_mfma_f32_16x16x128_f8f6f4 v[44:47], v[160:167], v[184:191], v[44:47]
	v_mfma_f32_16x16x128_f8f6f4 v[40:43], v[168:175], v[184:191], v[40:43]
	v_mfma_f32_16x16x128_f8f6f4 v[28:31], v[160:167], v[196:203], v[28:31]
	v_mfma_f32_16x16x128_f8f6f4 v[24:27], v[168:175], v[196:203], v[24:27]
	v_mfma_f32_16x16x128_f8f6f4 v[12:15], v[160:167], v[204:211], v[12:15]
	v_mfma_f32_16x16x128_f8f6f4 v[8:11], v[168:175], v[204:211], v[8:11]
	s_setprio 0
	s_barrier
	s_mov_b32 m0, s53
	v_lshl_add_u64 v[140:141], v[140:141], 0, s[16:17]
	global_load_lds_dwordx4 v[140:141], off
	v_lshl_add_u64 v[140:141], v[142:143], 0, s[16:17]
	s_mov_b32 m0, s54
	s_nop 0
	global_load_lds_dwordx4 v[140:141], off
	s_waitcnt vmcnt(4)
	s_waitcnt lgkmcnt(0)
	s_barrier
	s_setprio 1
	s_waitcnt lgkmcnt(0)
	v_mfma_f32_16x16x128_f8f6f4 v[52:55], v[218:225], v[176:183], v[52:55]
	v_mfma_f32_16x16x128_f8f6f4 v[48:51], v[226:233], v[176:183], v[48:51]
	v_mfma_f32_16x16x128_f8f6f4 v[36:39], v[218:225], v[184:191], v[36:39]
	v_mfma_f32_16x16x128_f8f6f4 v[32:35], v[226:233], v[184:191], v[32:35]
	v_mfma_f32_16x16x128_f8f6f4 v[20:23], v[218:225], v[196:203], v[20:23]
	v_mfma_f32_16x16x128_f8f6f4 v[16:19], v[226:233], v[196:203], v[16:19]
	v_mfma_f32_16x16x128_f8f6f4 v[4:7], v[218:225], v[204:211], v[4:7]
	v_mfma_f32_16x16x128_f8f6f4 v[0:3], v[226:233], v[204:211], v[0:3]
	s_setprio 0
	s_barrier
	s_mov_b32 m0, s57
	v_lshl_add_u64 v[140:141], s[34:35], 0, v[128:129]
	global_load_lds_dwordx4 v[140:141], off
	v_lshl_add_u64 v[140:141], s[34:35], 0, v[130:131]
	s_mov_b32 m0, s58
	s_andn2_b64 vcc, exec, s[28:29]
	global_load_lds_dwordx4 v[140:141], off
	s_mov_b64 s[30:31], -1
	s_mov_b64 s[28:29], 0
	s_mov_b64 s[34:35], 0x100
	s_cbranch_vccz .LBB0_1989
